# baseline (speedup 1.0000x reference)
.LBB1_1:
	s_and_b32 s0, s29, 0x10000
	v_add_u32_e32 v211, s0, v209
	v_add_u32_e32 v242, s0, v210
	ds_read_b128 v[212:215], v242 offset:0
	ds_read_b128 v[216:219], v242 offset:0x800
	ds_read_b128 v[220:223], v242 offset:0x1000
	ds_read_b128 v[224:227], v242 offset:0x1800
	ds_read_b128 v[228:231], v211 offset:0
	ds_read_b128 v[232:235], v211 offset:0x800
	ds_read_b128 v[236:239], v211 offset:0x1000
	s_nop 0
	s_waitcnt lgkmcnt(2)
	s_nop 0
	v_mfma_f32_16x16x32_bf16 v[174:177], v[212:215], v[228:231], v[174:177]
	v_mfma_f32_16x16x32_bf16 v[170:173], v[216:219], v[228:231], v[170:173]
	v_mfma_f32_16x16x32_bf16 v[166:169], v[220:223], v[228:231], v[166:169]
	v_mfma_f32_16x16x32_bf16 v[162:165], v[224:227], v[228:231], v[162:165]
	ds_read_b128 v[228:231], v211 offset:0x1800
	s_waitcnt lgkmcnt(2)
	s_nop 0
	v_mfma_f32_16x16x32_bf16 v[158:161], v[212:215], v[232:235], v[158:161]
	v_mfma_f32_16x16x32_bf16 v[154:157], v[216:219], v[232:235], v[154:157]
	v_mfma_f32_16x16x32_bf16 v[150:153], v[220:223], v[232:235], v[150:153]
	v_mfma_f32_16x16x32_bf16 v[146:149], v[224:227], v[232:235], v[146:149]
	ds_read_b128 v[232:235], v211 offset:0x2000
	s_waitcnt lgkmcnt(2)
	s_nop 0
	v_mfma_f32_16x16x32_bf16 v[142:145], v[212:215], v[236:239], v[142:145]
	v_mfma_f32_16x16x32_bf16 v[138:141], v[216:219], v[236:239], v[138:141]
	v_mfma_f32_16x16x32_bf16 v[134:137], v[220:223], v[236:239], v[134:137]
	v_mfma_f32_16x16x32_bf16 v[130:133], v[224:227], v[236:239], v[130:133]
	ds_read_b128 v[236:239], v211 offset:0x2800
	s_waitcnt lgkmcnt(2)
	s_nop 0
	v_mfma_f32_16x16x32_bf16 v[126:129], v[212:215], v[228:231], v[126:129]
	v_mfma_f32_16x16x32_bf16 v[122:125], v[216:219], v[228:231], v[122:125]
	v_mfma_f32_16x16x32_bf16 v[118:121], v[220:223], v[228:231], v[118:121]
	v_mfma_f32_16x16x32_bf16 v[114:117], v[224:227], v[228:231], v[114:117]
	ds_read_b128 v[228:231], v211 offset:0x3000
	s_waitcnt lgkmcnt(2)
	s_nop 0
	v_mfma_f32_16x16x32_bf16 v[110:113], v[212:215], v[232:235], v[110:113]
	v_mfma_f32_16x16x32_bf16 v[106:109], v[216:219], v[232:235], v[106:109]
	v_mfma_f32_16x16x32_bf16 v[102:105], v[220:223], v[232:235], v[102:105]
	v_mfma_f32_16x16x32_bf16 v[98:101], v[224:227], v[232:235], v[98:101]
	ds_read_b128 v[232:235], v211 offset:0x3800
	s_waitcnt lgkmcnt(2)
	s_nop 0
	v_mfma_f32_16x16x32_bf16 v[94:97], v[212:215], v[236:239], v[94:97]
	v_mfma_f32_16x16x32_bf16 v[90:93], v[216:219], v[236:239], v[90:93]
	v_mfma_f32_16x16x32_bf16 v[86:89], v[220:223], v[236:239], v[86:89]
	v_mfma_f32_16x16x32_bf16 v[82:85], v[224:227], v[236:239], v[82:85]
	s_waitcnt lgkmcnt(1)
	s_nop 0
	v_mfma_f32_16x16x32_bf16 v[78:81], v[212:215], v[228:231], v[78:81]
	v_mfma_f32_16x16x32_bf16 v[74:77], v[216:219], v[228:231], v[74:77]
	v_mfma_f32_16x16x32_bf16 v[70:73], v[220:223], v[228:231], v[70:73]
	v_mfma_f32_16x16x32_bf16 v[66:69], v[224:227], v[228:231], v[66:69]
	s_waitcnt lgkmcnt(0)
	s_nop 0
	v_mfma_f32_16x16x32_bf16 v[62:65], v[212:215], v[232:235], v[62:65]
	v_mfma_f32_16x16x32_bf16 v[58:61], v[216:219], v[232:235], v[58:61]
	v_mfma_f32_16x16x32_bf16 v[54:57], v[220:223], v[232:235], v[54:57]
	v_mfma_f32_16x16x32_bf16 v[50:53], v[224:227], v[232:235], v[50:53]
	s_xor_b32 s0, s0, 0x10000
	s_and_b32 s1, s22, 0x3c0
	s_add_i32 s23, s0, 0
	s_lshl_b32 s0, s1, 2
	s_add_u32 s20, s25, s0
	s_waitcnt vmcnt(10)
	v_cvt_pk_bf16_f32 v46, v46, v47
	v_cvt_pk_bf16_f32 v47, v48, v49
	v_cvt_pk_bf16_f32 v48, v42, v43
	v_cvt_pk_bf16_f32 v49, v44, v45
	s_waitcnt vmcnt(8)
	v_cvt_pk_bf16_f32 v38, v38, v39
	v_cvt_pk_bf16_f32 v39, v40, v41
	v_cvt_pk_bf16_f32 v40, v34, v35
	v_add_u32_e32 v34, s23, v208
	s_addc_u32 s21, s26, 0
	s_lshl_b32 s0, s1, 1
	v_cvt_pk_bf16_f32 v41, v36, v37
	v_lshlrev_b32_e32 v182, 2, v178
	v_add_u32_e32 v35, s23, v205
	v_add_u32_e32 v36, s23, v206
	v_add_u32_e32 v37, s23, v207
	ds_write_b128 v34, v[46:49]
	ds_write_b128 v35, v[38:41]
	s_waitcnt vmcnt(7)
	ds_write_b128 v36, v[30:33] offset:32768
	s_waitcnt vmcnt(6)
	ds_write_b128 v37, v[26:29] offset:32768
	v_lshl_add_u64 v[26:27], s[20:21], 0, v[180:181]
	v_lshl_add_u64 v[28:29], s[20:21], 0, v[184:185]
	s_add_u32 s0, s27, s0
	v_lshl_add_u64 v[26:27], v[26:27], 0, v[182:183]
	v_lshl_add_u64 v[28:29], v[28:29], 0, v[182:183]
	s_addc_u32 s1, s28, 0
	v_lshlrev_b32_e32 v240, 1, v178
	v_mov_b32_e32 v241, v183
	global_load_dwordx4 v[42:45], v[26:27], off offset:16
	global_load_dwordx4 v[46:49], v[26:27], off
	global_load_dwordx4 v[34:37], v[28:29], off offset:16
	global_load_dwordx4 v[38:41], v[28:29], off
	v_lshl_add_u64 v[26:27], s[0:1], 0, v[186:187]
	v_lshl_add_u64 v[28:29], s[0:1], 0, v[188:189]
	v_lshl_add_u64 v[26:27], v[26:27], 0, v[240:241]
	v_lshl_add_u64 v[28:29], v[28:29], 0, v[240:241]
	global_load_dwordx4 v[30:33], v[26:27], off
	s_nop 0
	global_load_dwordx4 v[26:29], v[28:29], off
	ds_read_b128 v[212:215], v242 offset:0x400
	ds_read_b128 v[216:219], v242 offset:0xc00
	ds_read_b128 v[220:223], v242 offset:0x1400
	ds_read_b128 v[224:227], v242 offset:0x1c00
	ds_read_b128 v[228:231], v211 offset:0x400
	ds_read_b128 v[232:235], v211 offset:0xc00
	ds_read_b128 v[236:239], v211 offset:0x1400
	s_nop 0
	s_waitcnt lgkmcnt(2)
	s_nop 0
	v_mfma_f32_16x16x32_bf16 v[174:177], v[212:215], v[228:231], v[174:177]
	v_mfma_f32_16x16x32_bf16 v[170:173], v[216:219], v[228:231], v[170:173]
	v_mfma_f32_16x16x32_bf16 v[166:169], v[220:223], v[228:231], v[166:169]
	v_mfma_f32_16x16x32_bf16 v[162:165], v[224:227], v[228:231], v[162:165]
	ds_read_b128 v[228:231], v211 offset:0x1c00
	s_waitcnt lgkmcnt(2)
	s_nop 0
	v_mfma_f32_16x16x32_bf16 v[158:161], v[212:215], v[232:235], v[158:161]
	v_mfma_f32_16x16x32_bf16 v[154:157], v[216:219], v[232:235], v[154:157]
	v_mfma_f32_16x16x32_bf16 v[150:153], v[220:223], v[232:235], v[150:153]
	v_mfma_f32_16x16x32_bf16 v[146:149], v[224:227], v[232:235], v[146:149]
	ds_read_b128 v[232:235], v211 offset:0x2400
	s_waitcnt lgkmcnt(2)
	s_nop 0
	v_mfma_f32_16x16x32_bf16 v[142:145], v[212:215], v[236:239], v[142:145]
	v_mfma_f32_16x16x32_bf16 v[138:141], v[216:219], v[236:239], v[138:141]
	v_mfma_f32_16x16x32_bf16 v[134:137], v[220:223], v[236:239], v[134:137]
	v_mfma_f32_16x16x32_bf16 v[130:133], v[224:227], v[236:239], v[130:133]
	ds_read_b128 v[236:239], v211 offset:0x2c00
	s_waitcnt lgkmcnt(2)
	s_nop 0
	v_mfma_f32_16x16x32_bf16 v[126:129], v[212:215], v[228:231], v[126:129]
	v_mfma_f32_16x16x32_bf16 v[122:125], v[216:219], v[228:231], v[122:125]
	v_mfma_f32_16x16x32_bf16 v[118:121], v[220:223], v[228:231], v[118:121]
	v_mfma_f32_16x16x32_bf16 v[114:117], v[224:227], v[228:231], v[114:117]
	ds_read_b128 v[228:231], v211 offset:0x3400
	s_waitcnt lgkmcnt(2)
	s_nop 0
	v_mfma_f32_16x16x32_bf16 v[110:113], v[212:215], v[232:235], v[110:113]
	v_mfma_f32_16x16x32_bf16 v[106:109], v[216:219], v[232:235], v[106:109]
	v_mfma_f32_16x16x32_bf16 v[102:105], v[220:223], v[232:235], v[102:105]
	v_mfma_f32_16x16x32_bf16 v[98:101], v[224:227], v[232:235], v[98:101]
	ds_read_b128 v[232:235], v211 offset:0x3c00
	s_waitcnt lgkmcnt(2)
	s_nop 0
	v_mfma_f32_16x16x32_bf16 v[94:97], v[212:215], v[236:239], v[94:97]
	v_mfma_f32_16x16x32_bf16 v[90:93], v[216:219], v[236:239], v[90:93]
	v_mfma_f32_16x16x32_bf16 v[86:89], v[220:223], v[236:239], v[86:89]
	v_mfma_f32_16x16x32_bf16 v[82:85], v[224:227], v[236:239], v[82:85]
	s_waitcnt lgkmcnt(1)
	s_nop 0
	v_mfma_f32_16x16x32_bf16 v[78:81], v[212:215], v[228:231], v[78:81]
	v_mfma_f32_16x16x32_bf16 v[74:77], v[216:219], v[228:231], v[74:77]
	v_mfma_f32_16x16x32_bf16 v[70:73], v[220:223], v[228:231], v[70:73]
	v_mfma_f32_16x16x32_bf16 v[66:69], v[224:227], v[228:231], v[66:69]
	s_waitcnt lgkmcnt(0)
	s_nop 0
	v_mfma_f32_16x16x32_bf16 v[62:65], v[212:215], v[232:235], v[62:65]
	v_mfma_f32_16x16x32_bf16 v[58:61], v[216:219], v[232:235], v[58:61]
	v_mfma_f32_16x16x32_bf16 v[54:57], v[220:223], v[232:235], v[54:57]
	v_mfma_f32_16x16x32_bf16 v[50:53], v[224:227], v[232:235], v[50:53]
	s_waitcnt vmcnt(10)
	v_cvt_pk_bf16_f32 v22, v22, v23
	v_cvt_pk_bf16_f32 v23, v24, v25
	v_cvt_pk_bf16_f32 v24, v6, v7
	v_cvt_pk_bf16_f32 v25, v8, v9
	v_add_u32_e32 v6, s23, v204
	s_waitcnt vmcnt(9)
	v_cvt_pk_bf16_f32 v8, v2, v3
	v_add_u32_e32 v2, s23, v201
	ds_write_b128 v6, v[22:25]
	s_waitcnt vmcnt(8)
	v_cvt_pk_bf16_f32 v6, v10, v11
	v_cvt_pk_bf16_f32 v7, v12, v13
	v_cvt_pk_bf16_f32 v9, v4, v5
	ds_write_b128 v2, v[6:9]
	v_add_u32_e32 v2, s23, v202
	s_waitcnt vmcnt(7)
	ds_write_b128 v2, v[18:21] offset:32768
	v_add_u32_e32 v2, s23, v203
	s_waitcnt vmcnt(6)
	ds_write_b128 v2, v[14:17] offset:32768
	v_lshl_add_u64 v[2:3], s[20:21], 0, v[190:191]
	v_lshl_add_u64 v[2:3], v[2:3], 0, v[182:183]
	global_load_dwordx4 v[6:9], v[2:3], off offset:16
	global_load_dwordx4 v[22:25], v[2:3], off
	v_lshl_add_u64 v[2:3], s[20:21], 0, v[192:193]
	v_lshl_add_u64 v[14:15], s[0:1], 0, v[194:195]
	v_lshl_add_u64 v[16:17], s[0:1], 0, v[196:197]
	v_lshl_add_u64 v[10:11], v[2:3], 0, v[182:183]
	v_lshl_add_u64 v[14:15], v[14:15], 0, v[240:241]
	v_lshl_add_u64 v[16:17], v[16:17], 0, v[240:241]
	global_load_dwordx4 v[2:5], v[10:11], off offset:16
	s_nop 0
	global_load_dwordx4 v[10:13], v[10:11], off
	s_nop 0
	global_load_dwordx4 v[18:21], v[14:15], off
	s_nop 0
	global_load_dwordx4 v[14:17], v[16:17], off
	s_waitcnt lgkmcnt(0)
	s_add_i32 s22, s22, 64
	s_add_i32 s29, s29, 0x10000
	s_cmp_lg_u32 s29, 0xe0000
	s_barrier
	s_cbranch_scc1 .LBB1_1
	s_lshl_b64 s[0:1], s[18:19], 24
	ds_read_b128 v[180:183], v210 offset:0
	ds_read_b128 v[184:187], v210 offset:0x800
	ds_read_b128 v[188:191], v210 offset:0x1000
	ds_read_b128 v[192:195], v210 offset:0x1800
	ds_read_b128 v[212:215], v209 offset:0
	ds_read_b128 v[216:219], v209 offset:0x800
	ds_read_b128 v[220:223], v209 offset:0x1000
	s_waitcnt lgkmcnt(0)
	s_add_u32 s0, s10, s0
	s_addc_u32 s18, s11, s1
	s_lshl_b32 s19, s24, 1
	s_mov_b32 s1, 0
	s_add_u32 s0, s0, s19
	s_waitcnt lgkmcnt(2)
	s_addc_u32 s20, s18, 0
	v_mfma_f32_16x16x32_bf16 v[174:177], v[180:183], v[212:215], v[174:177]
	v_mfma_f32_16x16x32_bf16 v[170:173], v[184:187], v[212:215], v[170:173]
	v_mfma_f32_16x16x32_bf16 v[166:169], v[188:191], v[212:215], v[166:169]
	v_mfma_f32_16x16x32_bf16 v[162:165], v[192:195], v[212:215], v[162:165]
	ds_read_b128 v[212:215], v209 offset:0x1800
	s_waitcnt lgkmcnt(2)
	s_nop 0
	v_mfma_f32_16x16x32_bf16 v[158:161], v[180:183], v[216:219], v[158:161]
	v_mfma_f32_16x16x32_bf16 v[154:157], v[184:187], v[216:219], v[154:157]
	v_mfma_f32_16x16x32_bf16 v[150:153], v[188:191], v[216:219], v[150:153]
	v_mfma_f32_16x16x32_bf16 v[146:149], v[192:195], v[216:219], v[146:149]
	ds_read_b128 v[216:219], v209 offset:0x2000
	s_waitcnt lgkmcnt(2)
	s_nop 0
	v_mfma_f32_16x16x32_bf16 v[142:145], v[180:183], v[220:223], v[142:145]
	v_mfma_f32_16x16x32_bf16 v[138:141], v[184:187], v[220:223], v[138:141]
	v_mfma_f32_16x16x32_bf16 v[134:137], v[188:191], v[220:223], v[134:137]
	v_mfma_f32_16x16x32_bf16 v[130:133], v[192:195], v[220:223], v[130:133]
	ds_read_b128 v[220:223], v209 offset:0x2800
	s_waitcnt lgkmcnt(2)
	s_nop 0
	v_mfma_f32_16x16x32_bf16 v[126:129], v[180:183], v[212:215], v[126:129]
	v_mfma_f32_16x16x32_bf16 v[122:125], v[184:187], v[212:215], v[122:125]
	v_mfma_f32_16x16x32_bf16 v[118:121], v[188:191], v[212:215], v[118:121]
	v_mfma_f32_16x16x32_bf16 v[114:117], v[192:195], v[212:215], v[114:117]
	ds_read_b128 v[212:215], v209 offset:0x3000
	s_waitcnt lgkmcnt(2)
	s_nop 0
	v_mfma_f32_16x16x32_bf16 v[110:113], v[180:183], v[216:219], v[110:113]
	v_mfma_f32_16x16x32_bf16 v[106:109], v[184:187], v[216:219], v[106:109]
	v_mfma_f32_16x16x32_bf16 v[102:105], v[188:191], v[216:219], v[102:105]
	v_mfma_f32_16x16x32_bf16 v[98:101], v[192:195], v[216:219], v[98:101]
	ds_read_b128 v[216:219], v209 offset:0x3800
	s_waitcnt lgkmcnt(2)
	s_nop 0
	v_mfma_f32_16x16x32_bf16 v[94:97], v[180:183], v[220:223], v[94:97]
	v_mfma_f32_16x16x32_bf16 v[90:93], v[184:187], v[220:223], v[90:93]
	v_mfma_f32_16x16x32_bf16 v[86:89], v[188:191], v[220:223], v[86:89]
	v_mfma_f32_16x16x32_bf16 v[82:85], v[192:195], v[220:223], v[82:85]
	s_waitcnt lgkmcnt(1)
	s_nop 0
	v_mfma_f32_16x16x32_bf16 v[78:81], v[180:183], v[212:215], v[78:81]
	v_mfma_f32_16x16x32_bf16 v[74:77], v[184:187], v[212:215], v[74:77]
	v_mfma_f32_16x16x32_bf16 v[70:73], v[188:191], v[212:215], v[70:73]
	v_mfma_f32_16x16x32_bf16 v[66:69], v[192:195], v[212:215], v[66:69]
	s_waitcnt lgkmcnt(0)
	s_nop 0
	v_mfma_f32_16x16x32_bf16 v[62:65], v[180:183], v[216:219], v[62:65]
	v_mfma_f32_16x16x32_bf16 v[58:61], v[184:187], v[216:219], v[58:61]
	v_mfma_f32_16x16x32_bf16 v[54:57], v[188:191], v[216:219], v[54:57]
	v_mfma_f32_16x16x32_bf16 v[50:53], v[192:195], v[216:219], v[50:53]
	s_add_i32 s18, 0, 0x10000
	s_waitcnt vmcnt(10)
	v_cvt_pk_bf16_f32 v46, v46, v47
	v_cvt_pk_bf16_f32 v47, v48, v49
	v_cvt_pk_bf16_f32 v48, v42, v43
	v_add_u32_e32 v42, s18, v208
	s_waitcnt vmcnt(8)
	v_cvt_pk_bf16_f32 v38, v38, v39
	v_cvt_pk_bf16_f32 v39, v40, v41
	v_cvt_pk_bf16_f32 v40, v34, v35
	v_add_u32_e32 v34, s18, v205
	s_add_i32 s19, 0, 0x18000
	v_cvt_pk_bf16_f32 v49, v44, v45
	ds_write_b128 v42, v[46:49]
	v_cvt_pk_bf16_f32 v41, v36, v37
	ds_write_b128 v34, v[38:41]
	v_add_u32_e32 v34, s19, v206
	s_waitcnt vmcnt(7)
	ds_write_b128 v34, v[30:33]
	v_add_u32_e32 v30, s19, v207
	s_waitcnt vmcnt(6)
	ds_write_b128 v30, v[26:29]
	ds_read_b128 v[26:29], v210 offset:0x400
	ds_read_b128 v[30:33], v210 offset:0xc00
	ds_read_b128 v[34:37], v210 offset:0x1400
	ds_read_b128 v[38:41], v210 offset:0x1c00
	ds_read_b128 v[42:45], v209 offset:0x400
	ds_read_b128 v[46:49], v209 offset:0xc00
	ds_read_b128 v[180:183], v209 offset:0x1400
	s_nop 0
	s_waitcnt lgkmcnt(2)
	s_nop 0
	v_mfma_f32_16x16x32_bf16 v[174:177], v[26:29], v[42:45], v[174:177]
	v_mfma_f32_16x16x32_bf16 v[170:173], v[30:33], v[42:45], v[170:173]
	v_mfma_f32_16x16x32_bf16 v[166:169], v[34:37], v[42:45], v[166:169]
	v_mfma_f32_16x16x32_bf16 v[42:45], v[38:41], v[42:45], v[162:165]
	ds_read_b128 v[162:165], v209 offset:0x1c00
	s_waitcnt lgkmcnt(2)
	s_nop 0
	v_mfma_f32_16x16x32_bf16 v[158:161], v[26:29], v[46:49], v[158:161]
	v_mfma_f32_16x16x32_bf16 v[154:157], v[30:33], v[46:49], v[154:157]
	v_mfma_f32_16x16x32_bf16 v[150:153], v[34:37], v[46:49], v[150:153]
	v_mfma_f32_16x16x32_bf16 v[46:49], v[38:41], v[46:49], v[146:149]
	ds_read_b128 v[146:149], v209 offset:0x2400
	s_waitcnt lgkmcnt(2)
	s_nop 0
	v_mfma_f32_16x16x32_bf16 v[142:145], v[26:29], v[180:183], v[142:145]
	v_mfma_f32_16x16x32_bf16 v[138:141], v[30:33], v[180:183], v[138:141]
	v_mfma_f32_16x16x32_bf16 v[134:137], v[34:37], v[180:183], v[134:137]
	v_mfma_f32_16x16x32_bf16 v[130:133], v[38:41], v[180:183], v[130:133]
	ds_read_b128 v[180:183], v209 offset:0x2c00
	s_waitcnt lgkmcnt(2)
	s_nop 0
	v_mfma_f32_16x16x32_bf16 v[126:129], v[26:29], v[162:165], v[126:129]
	v_mfma_f32_16x16x32_bf16 v[122:125], v[30:33], v[162:165], v[122:125]
	v_mfma_f32_16x16x32_bf16 v[118:121], v[34:37], v[162:165], v[118:121]
	v_mfma_f32_16x16x32_bf16 v[114:117], v[38:41], v[162:165], v[114:117]
	ds_read_b128 v[162:165], v209 offset:0x3400
	s_waitcnt lgkmcnt(2)
	s_nop 0
	v_mfma_f32_16x16x32_bf16 v[110:113], v[26:29], v[146:149], v[110:113]
	v_mfma_f32_16x16x32_bf16 v[106:109], v[30:33], v[146:149], v[106:109]
	v_mfma_f32_16x16x32_bf16 v[102:105], v[34:37], v[146:149], v[102:105]
	v_mfma_f32_16x16x32_bf16 v[98:101], v[38:41], v[146:149], v[98:101]
	ds_read_b128 v[146:149], v209 offset:0x3c00
	s_waitcnt lgkmcnt(2)
	s_nop 0
	v_mfma_f32_16x16x32_bf16 v[94:97], v[26:29], v[180:183], v[94:97]
	v_mfma_f32_16x16x32_bf16 v[90:93], v[30:33], v[180:183], v[90:93]
	v_mfma_f32_16x16x32_bf16 v[86:89], v[34:37], v[180:183], v[86:89]
	v_mfma_f32_16x16x32_bf16 v[82:85], v[38:41], v[180:183], v[82:85]
	s_waitcnt lgkmcnt(1)
	s_nop 0
	v_mfma_f32_16x16x32_bf16 v[78:81], v[26:29], v[162:165], v[78:81]
	v_mfma_f32_16x16x32_bf16 v[74:77], v[30:33], v[162:165], v[74:77]
	v_mfma_f32_16x16x32_bf16 v[70:73], v[34:37], v[162:165], v[70:73]
	v_mfma_f32_16x16x32_bf16 v[66:69], v[38:41], v[162:165], v[66:69]
	s_waitcnt lgkmcnt(0)
	s_nop 0
	v_mfma_f32_16x16x32_bf16 v[26:29], v[26:29], v[146:149], v[62:65]
	v_mfma_f32_16x16x32_bf16 v[30:33], v[30:33], v[146:149], v[58:61]
	v_mfma_f32_16x16x32_bf16 v[34:37], v[34:37], v[146:149], v[54:57]
	v_mfma_f32_16x16x32_bf16 v[38:41], v[38:41], v[146:149], v[50:53]
	s_waitcnt vmcnt(4)
	v_cvt_pk_bf16_f32 v22, v22, v23
	v_cvt_pk_bf16_f32 v23, v24, v25
	v_cvt_pk_bf16_f32 v24, v6, v7
	v_cvt_pk_bf16_f32 v25, v8, v9
	v_add_u32_e32 v6, s18, v204
	s_waitcnt vmcnt(3)
	v_cvt_pk_bf16_f32 v8, v2, v3
	v_add_u32_e32 v2, s18, v201
	ds_write_b128 v6, v[22:25]
	s_waitcnt vmcnt(2)
	v_cvt_pk_bf16_f32 v6, v10, v11
	v_cvt_pk_bf16_f32 v7, v12, v13
	v_cvt_pk_bf16_f32 v9, v4, v5
	ds_write_b128 v2, v[6:9]
	v_add_u32_e32 v2, s19, v202
	s_waitcnt vmcnt(1)
	ds_write_b128 v2, v[18:21]
	v_add_u32_e32 v2, s19, v203
	s_waitcnt vmcnt(0)
	ds_write_b128 v2, v[14:17]
	s_waitcnt lgkmcnt(0)
	s_barrier
	v_add_u32_e32 v178, 0x10000, v209
	v_add_u32_e32 v196, 0x10000, v210
	ds_read_b128 v[2:5], v196 offset:0
	ds_read_b128 v[6:9], v196 offset:0x800
	ds_read_b128 v[10:13], v196 offset:0x1000
	ds_read_b128 v[14:17], v196 offset:0x1800
	ds_read_b128 v[18:21], v178 offset:0
	s_and_b64 s[16:17], s[16:17], exec
	ds_read_b128 v[22:25], v178 offset:0x800
	ds_read_b128 v[50:53], v178 offset:0x1000
	s_waitcnt lgkmcnt(2)
	s_cselect_b32 s5, s5, s7
	s_cselect_b32 s4, s4, s6
	s_lshl_b32 s6, s3, 10
	v_mfma_f32_16x16x32_bf16 v[54:57], v[2:5], v[18:21], v[174:177]
	s_add_u32 s6, s4, s6
	s_addc_u32 s7, s5, 0
	s_lshl_b32 s3, s3, 9
	v_mfma_f32_16x16x32_bf16 v[58:61], v[6:9], v[18:21], v[170:173]
	s_add_u32 s4, s0, s3
	s_addc_u32 s5, s20, 0
	v_mfma_f32_16x16x32_bf16 v[62:65], v[10:13], v[18:21], v[166:169]
	v_mfma_f32_16x16x32_bf16 v[18:21], v[14:17], v[18:21], v[42:45]
	ds_read_b128 v[42:45], v178 offset:0x1800
	s_waitcnt lgkmcnt(2)
	s_nop 0
	v_mfma_f32_16x16x32_bf16 v[146:149], v[2:5], v[22:25], v[158:161]
	v_mfma_f32_16x16x32_bf16 v[154:157], v[6:9], v[22:25], v[154:157]
	v_mfma_f32_16x16x32_bf16 v[150:153], v[10:13], v[22:25], v[150:153]
	v_mfma_f32_16x16x32_bf16 v[22:25], v[14:17], v[22:25], v[46:49]
	ds_read_b128 v[46:49], v178 offset:0x2000
	s_waitcnt lgkmcnt(2)
	s_nop 0
	v_mfma_f32_16x16x32_bf16 v[142:145], v[2:5], v[50:53], v[142:145]
	v_mfma_f32_16x16x32_bf16 v[138:141], v[6:9], v[50:53], v[138:141]
	v_mfma_f32_16x16x32_bf16 v[134:137], v[10:13], v[50:53], v[134:137]
	v_mfma_f32_16x16x32_bf16 v[50:53], v[14:17], v[50:53], v[130:133]
	ds_read_b128 v[130:133], v178 offset:0x2800
	s_waitcnt lgkmcnt(2)
	s_nop 0
	v_mfma_f32_16x16x32_bf16 v[126:129], v[2:5], v[42:45], v[126:129]
	v_mfma_f32_16x16x32_bf16 v[122:125], v[6:9], v[42:45], v[122:125]
	v_mfma_f32_16x16x32_bf16 v[118:121], v[10:13], v[42:45], v[118:121]
	v_mfma_f32_16x16x32_bf16 v[42:45], v[14:17], v[42:45], v[114:117]
	ds_read_b128 v[114:117], v178 offset:0x3000
	s_waitcnt lgkmcnt(2)
	s_nop 0
	v_mfma_f32_16x16x32_bf16 v[110:113], v[2:5], v[46:49], v[110:113]
	v_mfma_f32_16x16x32_bf16 v[106:109], v[6:9], v[46:49], v[106:109]
	v_mfma_f32_16x16x32_bf16 v[102:105], v[10:13], v[46:49], v[102:105]
	v_mfma_f32_16x16x32_bf16 v[98:101], v[14:17], v[46:49], v[98:101]
	ds_read_b128 v[46:49], v178 offset:0x3800
	s_waitcnt lgkmcnt(2)
	s_nop 0
	v_mfma_f32_16x16x32_bf16 v[158:161], v[2:5], v[130:133], v[94:97]
	v_mfma_f32_16x16x32_bf16 v[162:165], v[6:9], v[130:133], v[90:93]
	v_mfma_f32_16x16x32_bf16 v[166:169], v[10:13], v[130:133], v[86:89]
	v_mfma_f32_16x16x32_bf16 v[130:133], v[14:17], v[130:133], v[82:85]
	s_waitcnt lgkmcnt(1)
	s_nop 0
	v_mfma_f32_16x16x32_bf16 v[66:69], v[14:17], v[114:117], v[66:69]
	v_mfma_f32_16x16x32_bf16 v[170:173], v[2:5], v[114:117], v[78:81]
	v_mfma_f32_16x16x32_bf16 v[174:177], v[6:9], v[114:117], v[74:77]
	v_mfma_f32_16x16x32_bf16 v[180:183], v[10:13], v[114:117], v[70:73]
	s_waitcnt lgkmcnt(0)
	s_nop 0
	v_mfma_f32_16x16x32_bf16 v[2:5], v[2:5], v[46:49], v[26:29]
	v_mfma_f32_16x16x32_bf16 v[114:117], v[6:9], v[46:49], v[30:33]
	v_mfma_f32_16x16x32_bf16 v[34:37], v[10:13], v[46:49], v[34:37]
	v_mfma_f32_16x16x32_bf16 v[184:187], v[14:17], v[46:49], v[38:41]
	ds_read_b128 v[188:191], v196 offset:0x400
	ds_read_b128 v[192:195], v196 offset:0xc00
	ds_read_b128 v[202:205], v196 offset:0x1400
	ds_read_b128 v[206:209], v196 offset:0x1c00
	ds_read_b128 v[6:9], v178 offset:0x400
	ds_read_b128 v[10:13], v178 offset:0xc00
	ds_read_b128 v[14:17], v178 offset:0x1400
	s_nop 0
	s_waitcnt lgkmcnt(2)
	s_nop 0
	v_mfma_f32_16x16x32_bf16 v[94:97], v[192:195], v[6:9], v[58:61]
	v_mfma_f32_16x16x32_bf16 v[62:65], v[202:205], v[6:9], v[62:65]
	v_mfma_f32_16x16x32_bf16 v[30:33], v[206:209], v[6:9], v[18:21]
	v_mfma_f32_16x16x32_bf16 v[210:213], v[188:191], v[6:9], v[54:57]
	ds_read_b128 v[6:9], v178 offset:0x1c00
	s_waitcnt lgkmcnt(2)
	s_nop 0
	v_mfma_f32_16x16x32_bf16 v[90:93], v[192:195], v[10:13], v[154:157]
	v_mfma_f32_16x16x32_bf16 v[58:61], v[202:205], v[10:13], v[150:153]
	v_mfma_f32_16x16x32_bf16 v[26:29], v[206:209], v[10:13], v[22:25]
	v_mfma_f32_16x16x32_bf16 v[146:149], v[188:191], v[10:13], v[146:149]
	ds_read_b128 v[10:13], v178 offset:0x2400
	s_waitcnt lgkmcnt(2)
	s_nop 0
	v_mfma_f32_16x16x32_bf16 v[86:89], v[192:195], v[14:17], v[138:141]
	v_mfma_f32_16x16x32_bf16 v[54:57], v[202:205], v[14:17], v[134:137]
	v_mfma_f32_16x16x32_bf16 v[22:25], v[206:209], v[14:17], v[50:53]
	v_mfma_f32_16x16x32_bf16 v[142:145], v[188:191], v[14:17], v[142:145]
	ds_read_b128 v[38:41], v178 offset:0x2c00
	s_waitcnt lgkmcnt(2)
	s_nop 0
	v_mfma_f32_16x16x32_bf16 v[126:129], v[188:191], v[6:9], v[126:129]
	v_mfma_f32_16x16x32_bf16 v[82:85], v[192:195], v[6:9], v[122:125]
	v_mfma_f32_16x16x32_bf16 v[50:53], v[202:205], v[6:9], v[118:121]
	v_mfma_f32_16x16x32_bf16 v[18:21], v[206:209], v[6:9], v[42:45]
	ds_read_b128 v[6:9], v178 offset:0x3400
	s_waitcnt lgkmcnt(2)
	s_nop 0
	v_mfma_f32_16x16x32_bf16 v[110:113], v[188:191], v[10:13], v[110:113]
	v_mfma_f32_16x16x32_bf16 v[78:81], v[192:195], v[10:13], v[106:109]
	v_mfma_f32_16x16x32_bf16 v[46:49], v[202:205], v[10:13], v[102:105]
	v_mfma_f32_16x16x32_bf16 v[14:17], v[206:209], v[10:13], v[98:101]
	ds_read_b128 v[98:101], v178 offset:0x3c00
	s_waitcnt lgkmcnt(2)
	s_nop 0
	v_mfma_f32_16x16x32_bf16 v[106:109], v[188:191], v[38:41], v[158:161]
	v_mfma_f32_16x16x32_bf16 v[74:77], v[192:195], v[38:41], v[162:165]
	v_mfma_f32_16x16x32_bf16 v[42:45], v[202:205], v[38:41], v[166:169]
	v_mfma_f32_16x16x32_bf16 v[10:13], v[206:209], v[38:41], v[130:133]
	s_waitcnt lgkmcnt(1)
	s_nop 0
	v_mfma_f32_16x16x32_bf16 v[118:121], v[188:191], v[6:9], v[170:173]
	v_mfma_f32_16x16x32_bf16 v[70:73], v[192:195], v[6:9], v[174:177]
	v_mfma_f32_16x16x32_bf16 v[38:41], v[202:205], v[6:9], v[180:183]
	v_mfma_f32_16x16x32_bf16 v[6:9], v[206:209], v[6:9], v[66:69]
	s_waitcnt lgkmcnt(0)
	s_nop 0
	v_mfma_f32_16x16x32_bf16 v[122:125], v[188:191], v[98:101], v[2:5]
	v_mfma_f32_16x16x32_bf16 v[66:69], v[192:195], v[98:101], v[114:117]
	v_mfma_f32_16x16x32_bf16 v[34:37], v[202:205], v[98:101], v[34:37]
	v_mfma_f32_16x16x32_bf16 v[2:5], v[206:209], v[98:101], v[184:187]
	v_lshrrev_b32_e32 v98, 2, v199
	v_and_b32_e32 v98, 12, v98
	v_lshl_or_b32 v104, v200, 6, v98
	v_lshlrev_b32_e32 v105, 2, v104
	s_waitcnt lgkmcnt(0)
	s_barrier
	global_load_dwordx4 v[114:117], v105, s[6:7]
	v_lshrrev_b32_e32 v98, 1, v199
	v_lshlrev_b32_e32 v99, 16, v198
	v_lshlrev_b32_e32 v100, 9, v179
	v_and_b32_e32 v102, 8, v98
	v_lshrrev_b32_e32 v98, 3, v104
	v_add3_u32 v103, 0, v99, v100
	v_xor_b32_e32 v130, v98, v179
	v_bitop3_b32 v131, v98, v179, 16 bitop3:0x1e
	global_load_dwordx4 v[98:101], v105, s[6:7] offset:64
	v_lshlrev_b32_e32 v130, 4, v130
	v_lshlrev_b32_e32 v131, 4, v131
	v_add3_u32 v130, v103, v130, v102
	v_add3_u32 v131, v103, v131, v102
	s_movk_i32 s0, 0x200
	s_waitcnt vmcnt(1)
	v_add_f32_e32 v132, v210, v114
	v_add_f32_e32 v133, v211, v115
	v_add_f32_e32 v134, v212, v116
	v_add_f32_e32 v135, v213, v117
	v_add_f32_e32 v140, v142, v114
	v_add_f32_e32 v141, v143, v115
	v_add_f32_e32 v142, v144, v116
	v_add_f32_e32 v143, v145, v117
	v_add_f32_e32 v110, v110, v114
	v_add_f32_e32 v111, v111, v115
	v_add_f32_e32 v106, v106, v114
	v_add_f32_e32 v107, v107, v115
	v_add_f32_e32 v136, v146, v114
	v_add_f32_e32 v137, v147, v115
	v_add_f32_e32 v138, v148, v116
	v_add_f32_e32 v139, v149, v117
	v_add_f32_e32 v126, v126, v114
	v_add_f32_e32 v127, v127, v115
	v_add_f32_e32 v128, v128, v116
	v_add_f32_e32 v129, v129, v117
	v_add_f32_e32 v112, v112, v116
	v_add_f32_e32 v113, v113, v117
	v_add_f32_e32 v108, v108, v116
	v_add_f32_e32 v109, v109, v117
	v_max_f32_e32 v132, 0, v132
	v_max_f32_e32 v133, 0, v133
	v_max_f32_e32 v134, 0, v134
	v_max_f32_e32 v135, 0, v135
	v_max_f32_e32 v140, 0, v140
	v_max_f32_e32 v141, 0, v141
	v_max_f32_e32 v142, 0, v142
	v_max_f32_e32 v143, 0, v143
	v_max_f32_e32 v144, 0, v110
	v_max_f32_e32 v145, 0, v111
	v_max_f32_e32 v148, 0, v106
	v_max_f32_e32 v149, 0, v107
	v_cvt_pk_bf16_f32 v106, v132, v133
	v_cvt_pk_bf16_f32 v107, v134, v135
	v_cvt_pk_bf16_f32 v110, v140, v141
	v_cvt_pk_bf16_f32 v111, v142, v143
	v_add_f32_e32 v118, v118, v114
	v_add_f32_e32 v119, v119, v115
	v_max_f32_e32 v136, 0, v136
	v_max_f32_e32 v137, 0, v137
	v_max_f32_e32 v138, 0, v138
	v_max_f32_e32 v139, 0, v139
	v_max_f32_e32 v126, 0, v126
	v_max_f32_e32 v127, 0, v127
	v_max_f32_e32 v128, 0, v128
	v_max_f32_e32 v129, 0, v129
	v_max_f32_e32 v146, 0, v112
	v_max_f32_e32 v147, 0, v113
	v_max_f32_e32 v150, 0, v108
	v_max_f32_e32 v151, 0, v109
	v_cvt_pk_bf16_f32 v108, v136, v137
	v_cvt_pk_bf16_f32 v109, v138, v139
	v_cvt_pk_bf16_f32 v112, v126, v127
	v_cvt_pk_bf16_f32 v113, v128, v129
	ds_write2st64_b64 v130, v[106:107], v[110:111] offset1:32
	ds_write2st64_b64 v131, v[108:109], v[112:113] offset0:16 offset1:48
	v_add_f32_e32 v106, v121, v117
	v_add_f32_e32 v120, v120, v116
	v_max_f32_e32 v152, 0, v118
	v_max_f32_e32 v153, 0, v119
	v_max_f32_e32 v107, 0, v106
	v_cvt_pk_bf16_f32 v106, v152, v153
	v_max_f32_e32 v120, 0, v120
	v_cvt_pk_bf16_f32 v118, v144, v145
	v_cvt_pk_bf16_f32 v119, v146, v147
	v_cvt_pk_bf16_f32 v107, v120, v107
	ds_write2st64_b64 v130, v[118:119], v[106:107] offset0:64 offset1:96
	v_add_f32_e32 v106, v122, v114
	v_max_f32_e32 v106, 0, v106
	v_add_f32_e32 v107, v123, v115
	v_max_f32_e32 v107, 0, v107
	v_add_f32_e32 v108, v124, v116
	v_add_f32_e32 v109, v125, v117
	v_cvt_pk_bf16_f32 v106, v106, v107
	v_cvt_pk_bf16_f32 v126, v148, v149
	v_cvt_pk_bf16_f32 v127, v150, v151
	v_max_f32_e32 v108, 0, v108
	v_max_f32_e32 v109, 0, v109
	v_cvt_pk_bf16_f32 v107, v108, v109
	ds_write2st64_b64 v131, v[126:127], v[106:107] offset0:80 offset1:112
	v_or_b32_e32 v106, 16, v104
	s_waitcnt vmcnt(0)
	v_add_f32_e32 v94, v94, v98
	v_add_f32_e32 v95, v95, v99
	v_add_f32_e32 v96, v96, v100
	v_lshrrev_b32_e32 v106, 3, v106
	v_max_f32_e32 v94, 0, v94
	v_max_f32_e32 v95, 0, v95
	v_max_f32_e32 v96, 0, v96
	v_add_f32_e32 v97, v97, v101
	v_max_f32_e32 v97, 0, v97
	v_cvt_pk_bf16_f32 v94, v94, v95
	v_cvt_pk_bf16_f32 v95, v96, v97
	v_xor_b32_e32 v96, v106, v179
	v_lshlrev_b32_e32 v96, 4, v96
	v_add3_u32 v107, v103, v96, v102
	v_add_f32_e32 v90, v90, v98
	v_add_f32_e32 v91, v91, v99
	v_add_f32_e32 v92, v92, v100
	ds_write_b64 v107, v[94:95]
	v_max_f32_e32 v90, 0, v90
	v_max_f32_e32 v91, 0, v91
	global_load_dwordx4 v[94:97], v105, s[6:7] offset:128
	v_max_f32_e32 v92, 0, v92
	v_add_f32_e32 v93, v93, v101
	v_max_f32_e32 v93, 0, v93
	v_cvt_pk_bf16_f32 v90, v90, v91
	v_cvt_pk_bf16_f32 v91, v92, v93
	v_bitop3_b32 v92, v106, v179, 16 bitop3:0x1e
	v_add_f32_e32 v66, v66, v98
	v_lshlrev_b32_e32 v92, 4, v92
	v_add_f32_e32 v86, v86, v98
	v_add_f32_e32 v87, v87, v99
	v_add_f32_e32 v82, v82, v98
	v_add_f32_e32 v83, v83, v99
	v_add_f32_e32 v78, v78, v98
	v_add_f32_e32 v79, v79, v99
	v_add_f32_e32 v74, v74, v98
	v_add_f32_e32 v75, v75, v99
	v_add_f32_e32 v70, v70, v98
	v_add_f32_e32 v71, v71, v99
	v_max_f32_e32 v66, 0, v66
	v_add_f32_e32 v67, v67, v99
	v_add3_u32 v92, v103, v92, v102
	v_max_f32_e32 v86, 0, v86
	v_max_f32_e32 v87, 0, v87
	v_add_f32_e32 v88, v88, v100
	v_add_f32_e32 v89, v89, v101
	v_max_f32_e32 v82, 0, v82
	v_max_f32_e32 v83, 0, v83
	v_add_f32_e32 v84, v84, v100
	v_add_f32_e32 v85, v85, v101
	v_max_f32_e32 v78, 0, v78
	v_max_f32_e32 v79, 0, v79
	v_add_f32_e32 v80, v80, v100
	v_add_f32_e32 v81, v81, v101
	v_max_f32_e32 v74, 0, v74
	v_max_f32_e32 v75, 0, v75
	v_add_f32_e32 v76, v76, v100
	v_add_f32_e32 v77, v77, v101
	v_max_f32_e32 v70, 0, v70
	v_max_f32_e32 v71, 0, v71
	v_add_f32_e32 v72, v72, v100
	v_add_f32_e32 v73, v73, v101
	v_max_f32_e32 v67, 0, v67
	v_add_f32_e32 v68, v68, v100
	v_add_f32_e32 v69, v69, v101
	v_cvt_pk_bf16_f32 v66, v66, v67
	ds_write_b64 v92, v[90:91] offset:8192
	v_max_f32_e32 v88, 0, v88
	v_max_f32_e32 v89, 0, v89
	v_cvt_pk_bf16_f32 v86, v86, v87
	v_cvt_pk_bf16_f32 v87, v88, v89
	ds_write_b64 v107, v[86:87] offset:16384
	v_max_f32_e32 v84, 0, v84
	v_max_f32_e32 v85, 0, v85
	v_cvt_pk_bf16_f32 v82, v82, v83
	v_cvt_pk_bf16_f32 v83, v84, v85
	ds_write_b64 v92, v[82:83] offset:24576
	v_max_f32_e32 v80, 0, v80
	v_max_f32_e32 v81, 0, v81
	v_cvt_pk_bf16_f32 v78, v78, v79
	v_cvt_pk_bf16_f32 v79, v80, v81
	ds_write_b64 v107, v[78:79] offset:32768
	v_max_f32_e32 v76, 0, v76
	v_max_f32_e32 v77, 0, v77
	v_cvt_pk_bf16_f32 v74, v74, v75
	v_cvt_pk_bf16_f32 v75, v76, v77
	ds_write_b64 v92, v[74:75] offset:40960
	v_max_f32_e32 v72, 0, v72
	v_max_f32_e32 v73, 0, v73
	v_cvt_pk_bf16_f32 v70, v70, v71
	v_cvt_pk_bf16_f32 v71, v72, v73
	ds_write_b64 v107, v[70:71] offset:49152
	v_max_f32_e32 v68, 0, v68
	v_max_f32_e32 v69, 0, v69
	v_cvt_pk_bf16_f32 v67, v68, v69
	ds_write_b64 v92, v[66:67] offset:57344
	v_or_b32_e32 v66, 32, v104
	v_lshrrev_b32_e32 v70, 3, v66
	global_load_dwordx4 v[66:69], v105, s[6:7] offset:192
	s_waitcnt vmcnt(1)
	v_add_f32_e32 v62, v62, v94
	v_add_f32_e32 v63, v63, v95
	v_add_f32_e32 v64, v64, v96
	v_add_f32_e32 v58, v58, v94
	v_add_f32_e32 v59, v59, v95
	v_add_f32_e32 v60, v60, v96
	v_max_f32_e32 v62, 0, v62
	v_max_f32_e32 v63, 0, v63
	v_max_f32_e32 v64, 0, v64
	v_add_f32_e32 v65, v65, v97
	v_max_f32_e32 v58, 0, v58
	v_max_f32_e32 v59, 0, v59
	v_max_f32_e32 v60, 0, v60
	v_add_f32_e32 v61, v61, v97
	v_max_f32_e32 v65, 0, v65
	v_cvt_pk_bf16_f32 v62, v62, v63
	v_cvt_pk_bf16_f32 v63, v64, v65
	v_xor_b32_e32 v64, v70, v179
	v_max_f32_e32 v61, 0, v61
	v_cvt_pk_bf16_f32 v58, v58, v59
	v_cvt_pk_bf16_f32 v59, v60, v61
	v_bitop3_b32 v60, v70, v179, 16 bitop3:0x1e
	v_add_f32_e32 v34, v34, v94
	v_lshlrev_b32_e32 v64, 4, v64
	v_lshlrev_b32_e32 v60, 4, v60
	v_add_f32_e32 v54, v54, v94
	v_add_f32_e32 v55, v55, v95
	v_add_f32_e32 v50, v50, v94
	v_add_f32_e32 v51, v51, v95
	v_add_f32_e32 v46, v46, v94
	v_add_f32_e32 v47, v47, v95
	v_add_f32_e32 v42, v42, v94
	v_add_f32_e32 v43, v43, v95
	v_add_f32_e32 v38, v38, v94
	v_add_f32_e32 v39, v39, v95
	v_max_f32_e32 v34, 0, v34
	v_add_f32_e32 v35, v35, v95
	v_add3_u32 v64, v103, v64, v102
	v_add3_u32 v60, v103, v60, v102
	v_max_f32_e32 v54, 0, v54
	v_max_f32_e32 v55, 0, v55
	v_add_f32_e32 v56, v56, v96
	v_add_f32_e32 v57, v57, v97
	v_max_f32_e32 v50, 0, v50
	v_max_f32_e32 v51, 0, v51
	v_add_f32_e32 v52, v52, v96
	v_add_f32_e32 v53, v53, v97
	v_max_f32_e32 v46, 0, v46
	v_max_f32_e32 v47, 0, v47
	v_add_f32_e32 v48, v48, v96
	v_add_f32_e32 v49, v49, v97
	v_max_f32_e32 v42, 0, v42
	v_max_f32_e32 v43, 0, v43
	v_add_f32_e32 v44, v44, v96
	v_add_f32_e32 v45, v45, v97
	v_max_f32_e32 v38, 0, v38
	v_max_f32_e32 v39, 0, v39
	v_add_f32_e32 v40, v40, v96
	v_add_f32_e32 v41, v41, v97
	v_max_f32_e32 v35, 0, v35
	v_add_f32_e32 v36, v36, v96
	v_add_f32_e32 v37, v37, v97
	v_cvt_pk_bf16_f32 v34, v34, v35
	ds_write_b64 v64, v[62:63]
	ds_write_b64 v60, v[58:59] offset:8192
	v_max_f32_e32 v56, 0, v56
	v_max_f32_e32 v57, 0, v57
	v_cvt_pk_bf16_f32 v54, v54, v55
	v_cvt_pk_bf16_f32 v55, v56, v57
	ds_write_b64 v64, v[54:55] offset:16384
	v_max_f32_e32 v52, 0, v52
	v_max_f32_e32 v53, 0, v53
	v_cvt_pk_bf16_f32 v50, v50, v51
	v_cvt_pk_bf16_f32 v51, v52, v53
	ds_write_b64 v60, v[50:51] offset:24576
	v_max_f32_e32 v48, 0, v48
	v_max_f32_e32 v49, 0, v49
	v_cvt_pk_bf16_f32 v46, v46, v47
	v_cvt_pk_bf16_f32 v47, v48, v49
	ds_write_b64 v64, v[46:47] offset:32768
	v_max_f32_e32 v44, 0, v44
	v_max_f32_e32 v45, 0, v45
	v_cvt_pk_bf16_f32 v42, v42, v43
	v_cvt_pk_bf16_f32 v43, v44, v45
	ds_write_b64 v60, v[42:43] offset:40960
	v_max_f32_e32 v40, 0, v40
	v_max_f32_e32 v41, 0, v41
	v_cvt_pk_bf16_f32 v38, v38, v39
	v_cvt_pk_bf16_f32 v39, v40, v41
	ds_write_b64 v64, v[38:39] offset:49152
	v_max_f32_e32 v36, 0, v36
	v_max_f32_e32 v37, 0, v37
	v_cvt_pk_bf16_f32 v35, v36, v37
	ds_write_b64 v60, v[34:35] offset:57344
	v_or_b32_e32 v34, 48, v104
	s_waitcnt vmcnt(0)
	v_add_f32_e32 v30, v30, v66
	v_add_f32_e32 v31, v31, v67
	v_add_f32_e32 v32, v32, v68
	v_add_f32_e32 v26, v26, v66
	v_add_f32_e32 v27, v27, v67
	v_add_f32_e32 v28, v28, v68
	v_lshrrev_b32_e32 v34, 3, v34
	v_max_f32_e32 v30, 0, v30
	v_max_f32_e32 v31, 0, v31
	v_max_f32_e32 v32, 0, v32
	v_add_f32_e32 v33, v33, v69
	v_max_f32_e32 v26, 0, v26
	v_max_f32_e32 v27, 0, v27
	v_max_f32_e32 v28, 0, v28
	v_add_f32_e32 v29, v29, v69
	v_max_f32_e32 v33, 0, v33
	v_cvt_pk_bf16_f32 v30, v30, v31
	v_cvt_pk_bf16_f32 v31, v32, v33
	v_xor_b32_e32 v32, v34, v179
	v_max_f32_e32 v29, 0, v29
	v_cvt_pk_bf16_f32 v26, v26, v27
	v_cvt_pk_bf16_f32 v27, v28, v29
	v_bitop3_b32 v28, v34, v179, 16 bitop3:0x1e
	v_add_f32_e32 v2, v2, v66
	v_lshlrev_b32_e32 v32, 4, v32
	v_lshlrev_b32_e32 v28, 4, v28
	v_add_f32_e32 v22, v22, v66
	v_add_f32_e32 v23, v23, v67
	v_add_f32_e32 v18, v18, v66
	v_add_f32_e32 v19, v19, v67
	v_add_f32_e32 v14, v14, v66
	v_add_f32_e32 v15, v15, v67
	v_add_f32_e32 v10, v10, v66
	v_add_f32_e32 v11, v11, v67
	v_add_f32_e32 v6, v6, v66
	v_add_f32_e32 v7, v7, v67
	v_max_f32_e32 v2, 0, v2
	v_add_f32_e32 v3, v3, v67
	v_add3_u32 v32, v103, v32, v102
	v_add3_u32 v28, v103, v28, v102
	v_max_f32_e32 v22, 0, v22
	v_max_f32_e32 v23, 0, v23
	v_add_f32_e32 v24, v24, v68
	v_add_f32_e32 v25, v25, v69
	v_max_f32_e32 v18, 0, v18
	v_max_f32_e32 v19, 0, v19
	v_add_f32_e32 v20, v20, v68
	v_add_f32_e32 v21, v21, v69
	v_max_f32_e32 v14, 0, v14
	v_max_f32_e32 v15, 0, v15
	v_add_f32_e32 v16, v16, v68
	v_add_f32_e32 v17, v17, v69
	v_max_f32_e32 v10, 0, v10
	v_max_f32_e32 v11, 0, v11
	v_add_f32_e32 v12, v12, v68
	v_add_f32_e32 v13, v13, v69
	v_max_f32_e32 v6, 0, v6
	v_max_f32_e32 v7, 0, v7
	v_add_f32_e32 v8, v8, v68
	v_add_f32_e32 v9, v9, v69
	v_max_f32_e32 v3, 0, v3
	v_add_f32_e32 v4, v4, v68
	v_add_f32_e32 v5, v5, v69
	v_cvt_pk_bf16_f32 v2, v2, v3
	ds_write_b64 v32, v[30:31]
	ds_write_b64 v28, v[26:27] offset:8192
	v_max_f32_e32 v24, 0, v24
	v_max_f32_e32 v25, 0, v25
	v_cvt_pk_bf16_f32 v22, v22, v23
	v_cvt_pk_bf16_f32 v23, v24, v25
	ds_write_b64 v32, v[22:23] offset:16384
	v_max_f32_e32 v20, 0, v20
	v_max_f32_e32 v21, 0, v21
	v_cvt_pk_bf16_f32 v18, v18, v19
	v_cvt_pk_bf16_f32 v19, v20, v21
	ds_write_b64 v28, v[18:19] offset:24576
	v_max_f32_e32 v16, 0, v16
	v_max_f32_e32 v17, 0, v17
	v_cvt_pk_bf16_f32 v14, v14, v15
	v_cvt_pk_bf16_f32 v15, v16, v17
	ds_write_b64 v32, v[14:15] offset:32768
	v_max_f32_e32 v12, 0, v12
	v_max_f32_e32 v13, 0, v13
	v_cvt_pk_bf16_f32 v10, v10, v11
	v_cvt_pk_bf16_f32 v11, v12, v13
	ds_write_b64 v28, v[10:11] offset:40960
	v_max_f32_e32 v8, 0, v8
	v_max_f32_e32 v9, 0, v9
	v_cvt_pk_bf16_f32 v6, v6, v7
	v_cvt_pk_bf16_f32 v7, v8, v9
	ds_write_b64 v32, v[6:7] offset:49152
	v_max_f32_e32 v4, 0, v4
	v_max_f32_e32 v5, 0, v5
	v_cvt_pk_bf16_f32 v3, v4, v5
	ds_write_b64 v28, v[2:3] offset:57344
	v_and_b32_e32 v2, 0x1f0, v1
	v_mov_b32_e32 v3, 0
	v_lshl_add_u64 v[12:13], s[4:5], 0, v[2:3]
	v_lshrrev_b32_e32 v1, 5, v0
	s_waitcnt lgkmcnt(0)
	s_barrier
	v_mov_b32_e32 v4, v1
	v_xor_b32_e32 v5, v4, v0
	v_lshlrev_b32_e32 v5, 4, v5
	v_and_b32_e32 v5, 0x1f0, v5
	v_lshl_add_u32 v6, v4, 9, v5
	ds_read_b128 v[192:195], v6
	v_lshlrev_b32_e32 v2, 11, v4
	v_lshl_add_u64 v[160:161], v[12:13], 0, v[2:3]
	v_or_b32_e32 v4, 0x10, v1
	v_xor_b32_e32 v5, v4, v0
	v_lshlrev_b32_e32 v5, 4, v5
	v_and_b32_e32 v5, 0x1f0, v5
	v_lshl_add_u32 v6, v4, 9, v5
	ds_read_b128 v[196:199], v6
	v_lshlrev_b32_e32 v2, 11, v4
	v_lshl_add_u64 v[162:163], v[12:13], 0, v[2:3]
	v_or_b32_e32 v4, 0x20, v1
	v_xor_b32_e32 v5, v4, v0
	v_lshlrev_b32_e32 v5, 4, v5
	v_and_b32_e32 v5, 0x1f0, v5
	v_lshl_add_u32 v6, v4, 9, v5
	ds_read_b128 v[200:203], v6
	v_lshlrev_b32_e32 v2, 11, v4
	v_lshl_add_u64 v[164:165], v[12:13], 0, v[2:3]
	v_or_b32_e32 v4, 0x30, v1
	v_xor_b32_e32 v5, v4, v0
	v_lshlrev_b32_e32 v5, 4, v5
	v_and_b32_e32 v5, 0x1f0, v5
	v_lshl_add_u32 v6, v4, 9, v5
	ds_read_b128 v[204:207], v6
	v_lshlrev_b32_e32 v2, 11, v4
	v_lshl_add_u64 v[166:167], v[12:13], 0, v[2:3]
	v_or_b32_e32 v4, 0x40, v1
	v_xor_b32_e32 v5, v4, v0
	v_lshlrev_b32_e32 v5, 4, v5
	v_and_b32_e32 v5, 0x1f0, v5
	v_lshl_add_u32 v6, v4, 9, v5
	ds_read_b128 v[208:211], v6
	v_lshlrev_b32_e32 v2, 11, v4
	v_lshl_add_u64 v[168:169], v[12:13], 0, v[2:3]
	v_or_b32_e32 v4, 0x50, v1
	v_xor_b32_e32 v5, v4, v0
	v_lshlrev_b32_e32 v5, 4, v5
	v_and_b32_e32 v5, 0x1f0, v5
	v_lshl_add_u32 v6, v4, 9, v5
	ds_read_b128 v[212:215], v6
	v_lshlrev_b32_e32 v2, 11, v4
	v_lshl_add_u64 v[170:171], v[12:13], 0, v[2:3]
	v_or_b32_e32 v4, 0x60, v1
	v_xor_b32_e32 v5, v4, v0
	v_lshlrev_b32_e32 v5, 4, v5
	v_and_b32_e32 v5, 0x1f0, v5
	v_lshl_add_u32 v6, v4, 9, v5
	ds_read_b128 v[216:219], v6
	v_lshlrev_b32_e32 v2, 11, v4
	v_lshl_add_u64 v[172:173], v[12:13], 0, v[2:3]
	v_or_b32_e32 v4, 0x70, v1
	v_xor_b32_e32 v5, v4, v0
	v_lshlrev_b32_e32 v5, 4, v5
	v_and_b32_e32 v5, 0x1f0, v5
	v_lshl_add_u32 v6, v4, 9, v5
	ds_read_b128 v[220:223], v6
	v_lshlrev_b32_e32 v2, 11, v4
	v_lshl_add_u64 v[174:175], v[12:13], 0, v[2:3]
	v_or_b32_e32 v4, 0x80, v1
	v_xor_b32_e32 v5, v4, v0
	v_lshlrev_b32_e32 v5, 4, v5
	v_and_b32_e32 v5, 0x1f0, v5
	v_lshl_add_u32 v6, v4, 9, v5
	ds_read_b128 v[224:227], v6
	v_lshlrev_b32_e32 v2, 11, v4
	v_lshl_add_u64 v[176:177], v[12:13], 0, v[2:3]
	v_or_b32_e32 v4, 0x90, v1
	v_xor_b32_e32 v5, v4, v0
	v_lshlrev_b32_e32 v5, 4, v5
	v_and_b32_e32 v5, 0x1f0, v5
	v_lshl_add_u32 v6, v4, 9, v5
	ds_read_b128 v[228:231], v6
	v_lshlrev_b32_e32 v2, 11, v4
	v_lshl_add_u64 v[178:179], v[12:13], 0, v[2:3]
	v_or_b32_e32 v4, 0xa0, v1
	v_xor_b32_e32 v5, v4, v0
	v_lshlrev_b32_e32 v5, 4, v5
	v_and_b32_e32 v5, 0x1f0, v5
	v_lshl_add_u32 v6, v4, 9, v5
	ds_read_b128 v[232:235], v6
	v_lshlrev_b32_e32 v2, 11, v4
	v_lshl_add_u64 v[180:181], v[12:13], 0, v[2:3]
	v_or_b32_e32 v4, 0xb0, v1
	v_xor_b32_e32 v5, v4, v0
	v_lshlrev_b32_e32 v5, 4, v5
	v_and_b32_e32 v5, 0x1f0, v5
	v_lshl_add_u32 v6, v4, 9, v5
	ds_read_b128 v[236:239], v6
	v_lshlrev_b32_e32 v2, 11, v4
	v_lshl_add_u64 v[182:183], v[12:13], 0, v[2:3]
	v_or_b32_e32 v4, 0xc0, v1
	v_xor_b32_e32 v5, v4, v0
	v_lshlrev_b32_e32 v5, 4, v5
	v_and_b32_e32 v5, 0x1f0, v5
	v_lshl_add_u32 v6, v4, 9, v5
	ds_read_b128 v[240:243], v6
	v_lshlrev_b32_e32 v2, 11, v4
	v_lshl_add_u64 v[184:185], v[12:13], 0, v[2:3]
	v_or_b32_e32 v4, 0xd0, v1
	v_xor_b32_e32 v5, v4, v0
	v_lshlrev_b32_e32 v5, 4, v5
	v_and_b32_e32 v5, 0x1f0, v5
	v_lshl_add_u32 v6, v4, 9, v5
	ds_read_b128 v[244:247], v6
	v_lshlrev_b32_e32 v2, 11, v4
	v_lshl_add_u64 v[186:187], v[12:13], 0, v[2:3]
	v_or_b32_e32 v4, 0xe0, v1
	v_xor_b32_e32 v5, v4, v0
	v_lshlrev_b32_e32 v5, 4, v5
	v_and_b32_e32 v5, 0x1f0, v5
	v_lshl_add_u32 v6, v4, 9, v5
	ds_read_b128 v[248:251], v6
	v_lshlrev_b32_e32 v2, 11, v4
	v_lshl_add_u64 v[188:189], v[12:13], 0, v[2:3]
	v_or_b32_e32 v4, 0xf0, v1
	v_xor_b32_e32 v5, v4, v0
	v_lshlrev_b32_e32 v5, 4, v5
	v_and_b32_e32 v5, 0x1f0, v5
	v_lshl_add_u32 v6, v4, 9, v5
	ds_read_b128 v[252:255], v6
	v_lshlrev_b32_e32 v2, 11, v4
	v_lshl_add_u64 v[190:191], v[12:13], 0, v[2:3]
	s_waitcnt lgkmcnt(15)
	global_store_dwordx4 v[160:161], v[192:195], off sc1
	s_waitcnt lgkmcnt(14)
	global_store_dwordx4 v[162:163], v[196:199], off sc1
	s_waitcnt lgkmcnt(13)
	global_store_dwordx4 v[164:165], v[200:203], off sc1
	s_waitcnt lgkmcnt(12)
	global_store_dwordx4 v[166:167], v[204:207], off sc1
	s_waitcnt lgkmcnt(11)
	global_store_dwordx4 v[168:169], v[208:211], off sc1
	s_waitcnt lgkmcnt(10)
	global_store_dwordx4 v[170:171], v[212:215], off sc1
	s_waitcnt lgkmcnt(9)
	global_store_dwordx4 v[172:173], v[216:219], off sc1
	s_waitcnt lgkmcnt(8)
	global_store_dwordx4 v[174:175], v[220:223], off sc1
	s_waitcnt lgkmcnt(7)
	global_store_dwordx4 v[176:177], v[224:227], off sc1
	s_waitcnt lgkmcnt(6)
	global_store_dwordx4 v[178:179], v[228:231], off sc1
	s_waitcnt lgkmcnt(5)
	global_store_dwordx4 v[180:181], v[232:235], off sc1
	s_waitcnt lgkmcnt(4)
	global_store_dwordx4 v[182:183], v[236:239], off sc1
	s_waitcnt lgkmcnt(3)
	global_store_dwordx4 v[184:185], v[240:243], off sc1
	s_waitcnt lgkmcnt(2)
	global_store_dwordx4 v[186:187], v[244:247], off sc1
	s_waitcnt lgkmcnt(1)
	global_store_dwordx4 v[188:189], v[248:251], off sc1
	s_waitcnt lgkmcnt(0)
	global_store_dwordx4 v[190:191], v[252:255], off sc1
	s_waitcnt lgkmcnt(0)
	s_barrier
	s_lshl_b32 s3, s2, 3
	s_and_b32 s3, s3, 56
	s_ashr_i32 s17, s2, 5
	s_add_i32 s20, s3, s17
	s_ashr_i32 s21, s20, 31
	s_bfe_u32 s16, s2, 0x20003
	s_lshl_b64 s[4:5], s[20:21], 17
	s_lshl_b64 s[6:7], s[20:21], 19
	s_add_u32 s6, s12, s6
	s_addc_u32 s7, s13, s7
	s_lshl_b32 s3, s16, 19
	s_add_u32 s3, s14, s3
	v_ashrrev_i32_e32 v2, 6, v0
	v_lshlrev_b32_e32 v1, 4, v0
	s_addc_u32 s13, s15, 0
	v_lshlrev_b32_e32 v4, 9, v2
	v_and_b32_e32 v5, 0x1f0, v1
	s_add_u32 s12, s3, 0x400000
	v_and_or_b32 v32, v4, s0, v5
	v_lshlrev_b32_e32 v4, 5, v2
	v_and_b32_e32 v5, 48, v1
	s_addc_u32 s13, s13, 0
	v_bitop3_b32 v4, v4, v5, 32 bitop3:0x6c
	s_and_b32 s15, s2, 8
	s_add_i32 s3, s20, 3
	v_bfe_u32 v31, v0, 5, 1
	v_lshrrev_b32_e32 v34, 1, v4
	v_add_u32_e32 v4, s15, v2
	s_mov_b32 s20, 0x3ffffe
	v_and_or_b32 v30, v4, s20, v31
	v_bfe_i32 v5, v30, 0, 22
	v_bfe_u32 v4, v30, 21, 1
	v_add_u32_e32 v6, v5, v4
	v_lshlrev_b32_e32 v4, 3, v6
	v_and_b32_e32 v6, 0x7fffffe, v6
	s_lshl_b32 s0, s17, 4
	v_sub_u32_e32 v5, v5, v6
	s_and_b32 s17, s0, 16
	v_lshl_or_b32 v6, v5, 5, v34
	v_add_u32_e32 v5, s17, v2
	v_and_or_b32 v35, v5, s20, v31
	v_bfe_i32 v7, v35, 0, 22
	v_bfe_u32 v8, v35, 21, 1
	v_add_u32_e32 v8, v7, v8
	v_lshlrev_b32_e32 v9, 3, v8
	v_and_b32_e32 v8, 0x7fffffe, v8
	v_add_u32_e32 v5, 8, v5
	v_sub_u32_e32 v7, v7, v8
	v_and_or_b32 v36, v5, s20, v31
	v_lshl_or_b32 v98, v7, 5, v34
	v_bfe_i32 v5, v36, 0, 22
	v_bfe_u32 v7, v36, 21, 1
	v_add_u32_e32 v7, v5, v7
	v_lshrrev_b32_e32 v33, 6, v32
	v_lshlrev_b32_e32 v8, 3, v7
	v_and_b32_e32 v7, 0x7fffffe, v7
	s_and_b32 s3, s3, 15
	v_and_or_b32 v4, v4, -16, v33
	v_sub_u32_e32 v5, v5, v7
	v_and_or_b32 v14, v9, -16, v33
	v_lshl_or_b32 v100, v5, 5, v34
	v_ashrrev_i32_e32 v5, 31, v4
	s_lshl_b32 s14, s3, 6
	s_lshl_b32 s0, s3, 8
	s_lshl_b32 s2, s3, 7
	v_and_or_b32 v16, v8, -16, v33
	v_lshlrev_b64 v[4:5], 12, v[4:5]
	s_add_u32 s2, s12, s2
	v_ashrrev_i32_e32 v15, 31, v14
	v_lshl_add_u64 v[4:5], s[6:7], 0, v[4:5]
	v_ashrrev_i32_e32 v7, 31, v6
	s_addc_u32 s3, s13, 0
	v_lshlrev_b64 v[102:103], 11, v[14:15]
	v_ashrrev_i32_e32 v99, 31, v98
	v_ashrrev_i32_e32 v17, 31, v16
	v_lshl_add_u64 v[8:9], v[4:5], 0, s[0:1]
	v_lshlrev_b64 v[38:39], 2, v[6:7]
	v_lshl_add_u64 v[14:15], s[2:3], 0, v[102:103]
	v_lshlrev_b64 v[22:23], 1, v[98:99]
	v_lshlrev_b64 v[104:105], 11, v[16:17]
	v_ashrrev_i32_e32 v101, 31, v100
	v_lshl_add_u64 v[18:19], v[8:9], 0, v[38:39]
	v_lshl_add_u64 v[24:25], v[14:15], 0, v[22:23]
	v_lshl_add_u64 v[14:15], s[2:3], 0, v[104:105]
	v_lshlrev_b64 v[26:27], 1, v[100:101]
	global_load_dwordx4 v[6:9], v[18:19], off offset:16
	global_load_dwordx4 v[10:13], v[18:19], off
	v_lshl_add_u64 v[28:29], v[14:15], 0, v[26:27]
	global_load_dwordx4 v[14:17], v[24:25], off
	global_load_dwordx4 v[18:21], v[28:29], off
	v_lshlrev_b32_e32 v24, 10, v30
	v_or_b32_e32 v125, v24, v32
	v_xad_u32 v24, s15, 8, v2
	v_and_or_b32 v24, v24, s20, v31
	v_lshlrev_b32_e32 v25, 10, v24
	v_or_b32_e32 v122, v25, v32
	v_bfe_i32 v25, v24, 0, 22
	v_bfe_u32 v24, v24, 21, 1
	v_add_u32_e32 v28, v25, v24
	v_lshlrev_b32_e32 v24, 3, v28
	v_and_b32_e32 v28, 0x7fffffe, v28
	v_sub_u32_e32 v25, v25, v28
	v_lshl_or_b32 v28, v25, 5, v34
	v_lshlrev_b32_e32 v25, 10, v35
	v_or_b32_e32 v126, v25, v32
	v_lshlrev_b32_e32 v25, 10, v36
	v_or_b32_e32 v127, v25, v32
	v_xad_u32 v25, s17, 16, v2
	v_and_or_b32 v25, v25, s20, v31
	v_lshlrev_b32_e32 v29, 10, v25
	v_or_b32_e32 v123, v29, v32
	v_bfe_i32 v29, v25, 0, 22
	v_bfe_u32 v25, v25, 21, 1
	v_add_u32_e32 v25, v29, v25
	v_and_b32_e32 v121, 3, v2
	v_lshlrev_b32_e32 v30, 3, v25
	v_and_b32_e32 v25, 0x7fffffe, v25
	v_xad_u32 v2, s17, 24, v2
	v_sub_u32_e32 v25, v29, v25
	v_and_or_b32 v2, v2, s20, v31
	v_lshl_or_b32 v106, v25, 5, v34
	v_lshlrev_b32_e32 v25, 10, v2
	v_or_b32_e32 v124, v25, v32
	v_bfe_i32 v25, v2, 0, 22
	v_bfe_u32 v2, v2, 21, 1
	v_add_u32_e32 v2, v25, v2
	v_lshlrev_b32_e32 v29, 3, v2
	v_and_b32_e32 v2, 0x7fffffe, v2
	v_and_b32_e32 v118, 15, v0
	v_sub_u32_e32 v2, v25, v2
	v_lshlrev_b32_e32 v25, 2, v0
	v_ashrrev_i32_e32 v120, 8, v0
	v_and_or_b32 v32, v29, -16, v33
	v_lshl_or_b32 v108, v2, 5, v34
	v_and_b32_e32 v2, 48, v0
	v_and_b32_e32 v25, 32, v25
	v_lshlrev_b32_e32 v29, 6, v118
	v_and_b32_e32 v119, 63, v0
	v_and_or_b32 v24, v24, -16, v33
	v_and_or_b32 v30, v30, -16, v33
	v_lshlrev_b32_e32 v68, 13, v120
	v_bitop3_b32 v2, v29, v25, v2 bitop3:0x36
	v_ashrrev_i32_e32 v25, 31, v24
	v_lshlrev_b64 v[24:25], 12, v[24:25]
	v_lshl_add_u64 v[56:57], s[6:7], 0, v[24:25]
	v_ashrrev_i32_e32 v29, 31, v28
	v_lshl_add_u64 v[24:25], v[56:57], 0, s[0:1]
	v_lshlrev_b64 v[58:59], 2, v[28:29]
	v_ashrrev_i32_e32 v31, 31, v30
	v_lshl_add_u64 v[24:25], v[24:25], 0, v[58:59]
	v_lshlrev_b64 v[110:111], 11, v[30:31]
	v_ashrrev_i32_e32 v107, 31, v106
	v_ashrrev_i32_e32 v33, 31, v32
	global_load_dwordx4 v[40:43], v[24:25], off offset:16
	global_load_dwordx4 v[44:47], v[24:25], off
	v_lshl_add_u64 v[24:25], s[2:3], 0, v[110:111]
	v_lshlrev_b64 v[60:61], 1, v[106:107]
	v_lshlrev_b64 v[112:113], 11, v[32:33]
	v_ashrrev_i32_e32 v109, 31, v108
	v_lshl_add_u64 v[24:25], v[24:25], 0, v[60:61]
	v_lshl_add_u64 v[28:29], s[2:3], 0, v[112:113]
	v_lshlrev_b64 v[62:63], 1, v[108:109]
	v_lshl_add_u64 v[28:29], v[28:29], 0, v[62:63]
	global_load_dwordx4 v[48:51], v[24:25], off
	global_load_dwordx4 v[52:55], v[28:29], off
	s_add_i32 s0, s14, 64
	s_and_b32 s2, s0, 0x3c0
	s_lshl_b32 s0, s2, 2
	s_lshl_b32 s2, s2, 1
	v_lshl_add_u64 v[24:25], v[4:5], 0, s[0:1]
	s_add_u32 s2, s12, s2
	v_lshl_add_u64 v[24:25], v[24:25], 0, v[38:39]
	s_addc_u32 s3, s13, 0
	global_load_dwordx4 v[30:33], v[24:25], off offset:16
	global_load_dwordx4 v[34:37], v[24:25], off
	v_lshl_add_u64 v[24:25], s[2:3], 0, v[102:103]
	v_lshl_add_u64 v[64:65], v[24:25], 0, v[22:23]
	v_lshl_add_u64 v[22:23], s[2:3], 0, v[104:105]
	v_lshl_add_u64 v[66:67], v[22:23], 0, v[26:27]
	global_load_dwordx4 v[26:29], v[64:65], off
	global_load_dwordx4 v[22:25], v[66:67], off
	v_add_u32_e32 v64, 0, v125
	s_waitcnt vmcnt(10)
	v_cvt_pk_bf16_f32 v10, v10, v11
	v_cvt_pk_bf16_f32 v11, v12, v13
	v_cvt_pk_bf16_f32 v12, v6, v7
	v_add_u32_e32 v6, 0, v126
	v_cvt_pk_bf16_f32 v13, v8, v9
	ds_write_b128 v64, v[10:13]
	s_waitcnt vmcnt(9)
	ds_write_b128 v6, v[14:17] offset:32768
	v_add_u32_e32 v6, 0, v127
	s_waitcnt vmcnt(8)
	ds_write_b128 v6, v[18:21] offset:32768
	v_add_u32_e32 v10, 0, v122
	s_waitcnt vmcnt(6)
	v_cvt_pk_bf16_f32 v6, v44, v45
	v_cvt_pk_bf16_f32 v7, v46, v47
	v_cvt_pk_bf16_f32 v8, v40, v41
	v_cvt_pk_bf16_f32 v9, v42, v43
	ds_write_b128 v10, v[6:9]
	v_add_u32_e32 v6, 0, v123
	s_waitcnt vmcnt(5)
	ds_write_b128 v6, v[48:51] offset:32768
	v_add_u32_e32 v6, 0, v124
	s_waitcnt vmcnt(4)
	ds_write_b128 v6, v[52:55] offset:32768
	v_lshl_add_u64 v[6:7], v[56:57], 0, s[0:1]
	v_lshl_add_u64 v[14:15], v[6:7], 0, v[58:59]
	global_load_dwordx4 v[6:9], v[14:15], off offset:16
	global_load_dwordx4 v[10:13], v[14:15], off
	v_lshl_add_u64 v[14:15], s[2:3], 0, v[110:111]
	v_lshl_add_u64 v[40:41], v[14:15], 0, v[60:61]
	v_lshl_add_u64 v[14:15], s[2:3], 0, v[112:113]
	v_lshl_add_u64 v[42:43], v[14:15], 0, v[62:63]
	global_load_dwordx4 v[18:21], v[40:41], off
	global_load_dwordx4 v[14:17], v[42:43], off
	v_lshlrev_b32_e32 v40, 13, v121
	s_cmp_lg_u32 0, -1
	s_waitcnt lgkmcnt(0)
	s_cselect_b32 s0, 0, 0
	v_add3_u32 v128, v68, s0, v2
	s_add_i32 s0, s0, 0x8000
	v_add3_u32 v129, v40, s0, v2
	v_lshl_add_u64 v[114:115], v[4:5], 0, v[38:39]
	v_lshl_add_u64 v[116:117], v[56:57], 0, v[58:59]
	s_add_i32 s2, s14, 0x80
	s_mov_b32 s3, 0
	v_mov_b32_e32 v2, v3
	v_mov_b32_e32 v4, v3
	v_mov_b32_e32 v5, v3
	v_mov_b32_e32 v38, v3
	v_mov_b32_e32 v39, v3
	v_mov_b32_e32 v40, v3
	v_mov_b32_e32 v41, v3
	v_mov_b32_e32 v42, v3
	v_mov_b32_e32 v43, v3
	v_mov_b32_e32 v44, v3
	v_mov_b32_e32 v45, v3
	v_mov_b32_e32 v46, v3
	v_mov_b32_e32 v47, v3
	v_mov_b32_e32 v48, v3
	v_mov_b32_e32 v49, v3
	v_mov_b32_e32 v50, v3
	v_mov_b32_e32 v51, v3
	v_mov_b32_e32 v52, v3
	v_mov_b32_e32 v53, v3
	v_mov_b32_e32 v54, v3
	v_mov_b32_e32 v55, v3
	v_mov_b32_e32 v56, v3
	v_mov_b32_e32 v57, v3
	v_mov_b32_e32 v58, v3
	v_mov_b32_e32 v59, v3
	v_mov_b32_e32 v60, v3
	v_mov_b32_e32 v61, v3
	v_mov_b32_e32 v62, v3
	v_mov_b32_e32 v63, v3
	v_mov_b32_e32 v64, v3
	v_mov_b32_e32 v65, v3
	v_mov_b32_e32 v66, v3
	v_mov_b32_e32 v67, v3
	v_mov_b32_e32 v68, v3
	v_mov_b32_e32 v69, v3
	v_mov_b32_e32 v70, v3
	v_mov_b32_e32 v71, v3
	v_mov_b32_e32 v72, v3
	v_mov_b32_e32 v73, v3
	v_mov_b32_e32 v74, v3
	v_mov_b32_e32 v75, v3
	v_mov_b32_e32 v76, v3
	v_mov_b32_e32 v77, v3
	v_mov_b32_e32 v78, v3
	v_mov_b32_e32 v79, v3
	v_mov_b32_e32 v80, v3
	v_mov_b32_e32 v81, v3
	v_mov_b32_e32 v82, v3
	v_mov_b32_e32 v83, v3
	v_mov_b32_e32 v84, v3
	v_mov_b32_e32 v85, v3
	v_mov_b32_e32 v86, v3
	v_mov_b32_e32 v87, v3
	v_mov_b32_e32 v88, v3
	v_mov_b32_e32 v89, v3
	v_mov_b32_e32 v90, v3
	v_mov_b32_e32 v91, v3
	v_mov_b32_e32 v92, v3
	v_mov_b32_e32 v93, v3
	v_mov_b32_e32 v94, v3
	v_mov_b32_e32 v95, v3
	v_mov_b32_e32 v96, v3
	v_mov_b32_e32 v97, v3
	s_barrier
.LBB1_3:
	s_and_b32 s0, s3, 0x10000
	v_add_u32_e32 v158, s0, v128
	v_add_u32_e32 v159, s0, v129
	ds_read_b128 v[130:133], v159 offset:0
	ds_read_b128 v[134:137], v159 offset:0x800
	ds_read_b128 v[138:141], v159 offset:0x1000
	ds_read_b128 v[142:145], v159 offset:0x1800
	ds_read_b128 v[146:149], v158 offset:0
	ds_read_b128 v[150:153], v158 offset:0x800
	ds_read_b128 v[154:157], v158 offset:0x1000
	s_nop 0
	s_waitcnt lgkmcnt(2)
	s_nop 0
	v_mfma_f32_16x16x32_bf16 v[94:97], v[130:133], v[146:149], v[94:97]
	v_mfma_f32_16x16x32_bf16 v[90:93], v[134:137], v[146:149], v[90:93]
	v_mfma_f32_16x16x32_bf16 v[86:89], v[138:141], v[146:149], v[86:89]
	v_mfma_f32_16x16x32_bf16 v[82:85], v[142:145], v[146:149], v[82:85]
	ds_read_b128 v[146:149], v158 offset:0x1800
	s_waitcnt lgkmcnt(2)
	s_nop 0
	v_mfma_f32_16x16x32_bf16 v[78:81], v[130:133], v[150:153], v[78:81]
	v_mfma_f32_16x16x32_bf16 v[74:77], v[134:137], v[150:153], v[74:77]
	v_mfma_f32_16x16x32_bf16 v[70:73], v[138:141], v[150:153], v[70:73]
	v_mfma_f32_16x16x32_bf16 v[66:69], v[142:145], v[150:153], v[66:69]
	s_waitcnt lgkmcnt(1)
	s_nop 0
	v_mfma_f32_16x16x32_bf16 v[62:65], v[130:133], v[154:157], v[62:65]
	v_mfma_f32_16x16x32_bf16 v[58:61], v[134:137], v[154:157], v[58:61]
	v_mfma_f32_16x16x32_bf16 v[54:57], v[138:141], v[154:157], v[54:57]
	v_mfma_f32_16x16x32_bf16 v[50:53], v[142:145], v[154:157], v[50:53]
	s_waitcnt lgkmcnt(0)
	s_nop 0
	v_mfma_f32_16x16x32_bf16 v[46:49], v[130:133], v[146:149], v[46:49]
	v_mfma_f32_16x16x32_bf16 v[42:45], v[134:137], v[146:149], v[42:45]
	v_mfma_f32_16x16x32_bf16 v[38:41], v[138:141], v[146:149], v[38:41]
	v_mfma_f32_16x16x32_bf16 v[2:5], v[142:145], v[146:149], v[2:5]
	s_xor_b32 s0, s0, 0x10000
	s_and_b32 s6, s2, 0x3c0
	s_add_i32 s14, s0, 0
	s_lshl_b32 s0, s6, 2
	s_lshl_b32 s6, s6, 1
	s_add_u32 s6, s12, s6
	s_waitcnt vmcnt(6)
	v_cvt_pk_bf16_f32 v34, v34, v35
	v_cvt_pk_bf16_f32 v35, v36, v37
	v_cvt_pk_bf16_f32 v36, v30, v31
	v_cvt_pk_bf16_f32 v37, v32, v33
	v_add_u32_e32 v30, s14, v125
	s_addc_u32 s7, s13, 0
	v_add_u32_e32 v31, s14, v126
	v_add_u32_e32 v32, s14, v127
	ds_write_b128 v30, v[34:37]
	s_waitcnt vmcnt(5)
	ds_write_b128 v31, v[26:29] offset:32768
	s_waitcnt vmcnt(4)
	ds_write_b128 v32, v[22:25] offset:32768
	v_lshl_add_u64 v[22:23], s[6:7], 0, v[102:103]
	v_lshl_add_u64 v[24:25], s[6:7], 0, v[104:105]
	v_lshl_add_u64 v[130:131], v[114:115], 0, s[0:1]
	v_lshl_add_u64 v[22:23], v[98:99], 1, v[22:23]
	v_lshl_add_u64 v[24:25], v[100:101], 1, v[24:25]
	global_load_dwordx4 v[30:33], v[130:131], off offset:16
	global_load_dwordx4 v[34:37], v[130:131], off
	global_load_dwordx4 v[26:29], v[22:23], off
	s_nop 0
	global_load_dwordx4 v[22:25], v[24:25], off
	ds_read_b128 v[130:133], v159 offset:0x400
	ds_read_b128 v[134:137], v159 offset:0xc00
	ds_read_b128 v[138:141], v159 offset:0x1400
	ds_read_b128 v[142:145], v159 offset:0x1c00
	ds_read_b128 v[146:149], v158 offset:0x400
	ds_read_b128 v[150:153], v158 offset:0xc00
	ds_read_b128 v[154:157], v158 offset:0x1400
	s_nop 0
	s_waitcnt lgkmcnt(2)
	s_nop 0
	v_mfma_f32_16x16x32_bf16 v[94:97], v[130:133], v[146:149], v[94:97]
	v_mfma_f32_16x16x32_bf16 v[90:93], v[134:137], v[146:149], v[90:93]
	v_mfma_f32_16x16x32_bf16 v[86:89], v[138:141], v[146:149], v[86:89]
	v_mfma_f32_16x16x32_bf16 v[82:85], v[142:145], v[146:149], v[82:85]
	ds_read_b128 v[146:149], v158 offset:0x1c00
	s_waitcnt lgkmcnt(2)
	s_nop 0
	v_mfma_f32_16x16x32_bf16 v[78:81], v[130:133], v[150:153], v[78:81]
	v_mfma_f32_16x16x32_bf16 v[74:77], v[134:137], v[150:153], v[74:77]
	v_mfma_f32_16x16x32_bf16 v[70:73], v[138:141], v[150:153], v[70:73]
	v_mfma_f32_16x16x32_bf16 v[66:69], v[142:145], v[150:153], v[66:69]
	s_waitcnt lgkmcnt(1)
	s_nop 0
	v_mfma_f32_16x16x32_bf16 v[62:65], v[130:133], v[154:157], v[62:65]
	v_mfma_f32_16x16x32_bf16 v[58:61], v[134:137], v[154:157], v[58:61]
	v_mfma_f32_16x16x32_bf16 v[54:57], v[138:141], v[154:157], v[54:57]
	v_mfma_f32_16x16x32_bf16 v[50:53], v[142:145], v[154:157], v[50:53]
	s_waitcnt lgkmcnt(0)
	s_nop 0
	v_mfma_f32_16x16x32_bf16 v[46:49], v[130:133], v[146:149], v[46:49]
	v_mfma_f32_16x16x32_bf16 v[42:45], v[134:137], v[146:149], v[42:45]
	v_mfma_f32_16x16x32_bf16 v[38:41], v[138:141], v[146:149], v[38:41]
	v_mfma_f32_16x16x32_bf16 v[2:5], v[142:145], v[146:149], v[2:5]
	v_add_u32_e32 v130, s14, v122
	s_waitcnt vmcnt(6)
	v_cvt_pk_bf16_f32 v10, v10, v11
	v_cvt_pk_bf16_f32 v11, v12, v13
	v_cvt_pk_bf16_f32 v12, v6, v7
	v_add_u32_e32 v6, s14, v123
	v_cvt_pk_bf16_f32 v13, v8, v9
	ds_write_b128 v130, v[10:13]
	s_waitcnt vmcnt(5)
	ds_write_b128 v6, v[18:21] offset:32768
	v_add_u32_e32 v6, s14, v124
	s_waitcnt vmcnt(4)
	ds_write_b128 v6, v[14:17] offset:32768
	v_lshl_add_u64 v[14:15], s[6:7], 0, v[110:111]
	v_lshl_add_u64 v[16:17], s[6:7], 0, v[112:113]
	v_lshl_add_u64 v[10:11], v[116:117], 0, s[0:1]
	v_lshl_add_u64 v[14:15], v[106:107], 1, v[14:15]
	v_lshl_add_u64 v[16:17], v[108:109], 1, v[16:17]
	global_load_dwordx4 v[6:9], v[10:11], off offset:16
	s_nop 0
	global_load_dwordx4 v[10:13], v[10:11], off
	s_nop 0
	global_load_dwordx4 v[18:21], v[14:15], off
	s_nop 0
	global_load_dwordx4 v[14:17], v[16:17], off
	s_waitcnt lgkmcnt(0)
	s_add_i32 s2, s2, 64
	s_add_i32 s3, s3, 0x10000
	s_cmp_lg_u32 s3, 0xe0000
	s_barrier
	s_cbranch_scc1 .LBB1_3
	ds_read_b128 v[98:101], v129 offset:0
	ds_read_b128 v[102:105], v129 offset:0x800
	ds_read_b128 v[106:109], v129 offset:0x1000
	ds_read_b128 v[110:113], v129 offset:0x1800
	ds_read_b128 v[114:117], v128 offset:0
	ds_read_b128 v[130:133], v128 offset:0x800
	ds_read_b128 v[134:137], v128 offset:0x1000
	s_nop 0
	s_waitcnt lgkmcnt(2)
	s_nop 0
	v_mfma_f32_16x16x32_bf16 v[94:97], v[98:101], v[114:117], v[94:97]
	v_mfma_f32_16x16x32_bf16 v[90:93], v[102:105], v[114:117], v[90:93]
	v_mfma_f32_16x16x32_bf16 v[86:89], v[106:109], v[114:117], v[86:89]
	v_mfma_f32_16x16x32_bf16 v[82:85], v[110:113], v[114:117], v[82:85]
	ds_read_b128 v[114:117], v128 offset:0x1800
	s_waitcnt lgkmcnt(2)
	s_nop 0
	v_mfma_f32_16x16x32_bf16 v[78:81], v[98:101], v[130:133], v[78:81]
	v_mfma_f32_16x16x32_bf16 v[74:77], v[102:105], v[130:133], v[74:77]
	v_mfma_f32_16x16x32_bf16 v[70:73], v[106:109], v[130:133], v[70:73]
	v_mfma_f32_16x16x32_bf16 v[66:69], v[110:113], v[130:133], v[66:69]
	s_waitcnt lgkmcnt(1)
	s_nop 0
	v_mfma_f32_16x16x32_bf16 v[62:65], v[98:101], v[134:137], v[62:65]
	v_mfma_f32_16x16x32_bf16 v[58:61], v[102:105], v[134:137], v[58:61]
	v_mfma_f32_16x16x32_bf16 v[54:57], v[106:109], v[134:137], v[54:57]
	v_mfma_f32_16x16x32_bf16 v[50:53], v[110:113], v[134:137], v[50:53]
	s_waitcnt lgkmcnt(0)
	s_nop 0
	v_mfma_f32_16x16x32_bf16 v[46:49], v[98:101], v[114:117], v[46:49]
	v_mfma_f32_16x16x32_bf16 v[42:45], v[102:105], v[114:117], v[42:45]
	v_mfma_f32_16x16x32_bf16 v[38:41], v[106:109], v[114:117], v[38:41]
	v_mfma_f32_16x16x32_bf16 v[2:5], v[110:113], v[114:117], v[2:5]
	v_add_u32_e32 v98, s18, v125
	s_waitcnt vmcnt(6)
	v_cvt_pk_bf16_f32 v34, v34, v35
	v_cvt_pk_bf16_f32 v35, v36, v37
	v_cvt_pk_bf16_f32 v36, v30, v31
	v_add_u32_e32 v30, s19, v126
	v_cvt_pk_bf16_f32 v37, v32, v33
	ds_write_b128 v98, v[34:37]
	s_waitcnt vmcnt(5)
	ds_write_b128 v30, v[26:29]
	v_add_u32_e32 v26, s19, v127
	s_waitcnt vmcnt(4)
	ds_write_b128 v26, v[22:25]
	ds_read_b128 v[22:25], v129 offset:0x400
	ds_read_b128 v[26:29], v129 offset:0xc00
	ds_read_b128 v[30:33], v129 offset:0x1400
	ds_read_b128 v[34:37], v129 offset:0x1c00
	ds_read_b128 v[98:101], v128 offset:0x400
	ds_read_b128 v[102:105], v128 offset:0xc00
	ds_read_b128 v[106:109], v128 offset:0x1400
	s_nop 0
	s_waitcnt lgkmcnt(2)
	s_nop 0
	v_mfma_f32_16x16x32_bf16 v[94:97], v[22:25], v[98:101], v[94:97]
	v_mfma_f32_16x16x32_bf16 v[90:93], v[26:29], v[98:101], v[90:93]
	v_mfma_f32_16x16x32_bf16 v[86:89], v[30:33], v[98:101], v[86:89]
	v_mfma_f32_16x16x32_bf16 v[82:85], v[34:37], v[98:101], v[82:85]
	ds_read_b128 v[98:101], v128 offset:0x1c00
	s_waitcnt lgkmcnt(2)
	s_nop 0
	v_mfma_f32_16x16x32_bf16 v[78:81], v[22:25], v[102:105], v[78:81]
	v_mfma_f32_16x16x32_bf16 v[74:77], v[26:29], v[102:105], v[74:77]
	v_mfma_f32_16x16x32_bf16 v[70:73], v[30:33], v[102:105], v[70:73]
	v_mfma_f32_16x16x32_bf16 v[66:69], v[34:37], v[102:105], v[66:69]
	s_waitcnt lgkmcnt(1)
	s_nop 0
	v_mfma_f32_16x16x32_bf16 v[62:65], v[22:25], v[106:109], v[62:65]
	v_mfma_f32_16x16x32_bf16 v[58:61], v[26:29], v[106:109], v[58:61]
	v_mfma_f32_16x16x32_bf16 v[54:57], v[30:33], v[106:109], v[54:57]
	v_mfma_f32_16x16x32_bf16 v[50:53], v[34:37], v[106:109], v[50:53]
	s_waitcnt lgkmcnt(0)
	s_nop 0
	v_mfma_f32_16x16x32_bf16 v[22:25], v[22:25], v[98:101], v[46:49]
	v_mfma_f32_16x16x32_bf16 v[26:29], v[26:29], v[98:101], v[42:45]
	v_mfma_f32_16x16x32_bf16 v[30:33], v[30:33], v[98:101], v[38:41]
	v_mfma_f32_16x16x32_bf16 v[2:5], v[34:37], v[98:101], v[2:5]
	v_add_u32_e32 v34, s18, v122
	s_waitcnt vmcnt(2)
	v_cvt_pk_bf16_f32 v10, v10, v11
	v_cvt_pk_bf16_f32 v11, v12, v13
	v_cvt_pk_bf16_f32 v12, v6, v7
	v_add_u32_e32 v6, s19, v123
	s_lshl_b64 s[0:1], s[4:5], 1
	v_cvt_pk_bf16_f32 v13, v8, v9
	ds_write_b128 v34, v[10:13]
	s_waitcnt vmcnt(1)
	ds_write_b128 v6, v[18:21]
	v_add_u32_e32 v6, s19, v124
	s_add_u32 s0, s10, s0
	s_waitcnt vmcnt(0)
	ds_write_b128 v6, v[14:17]
	s_addc_u32 s1, s11, s1
	s_lshl_b32 s2, s16, 9
	s_waitcnt lgkmcnt(0)
	s_barrier
	v_add_u32_e32 v110, 0x10000, v128
	v_add_u32_e32 v102, 0x10000, v129
	ds_read_b128 v[6:9], v102 offset:0
	ds_read_b128 v[10:13], v102 offset:0x800
	ds_read_b128 v[14:17], v102 offset:0x1000
	ds_read_b128 v[18:21], v102 offset:0x1800
	ds_read_b128 v[34:37], v110 offset:0
	ds_read_b128 v[38:41], v110 offset:0x800
	ds_read_b128 v[42:45], v110 offset:0x1000
	s_add_u32 s0, s0, s2
	s_addc_u32 s1, s1, 0
	s_lshl_b32 s2, s16, 10
	s_waitcnt lgkmcnt(2)
	s_add_u32 s2, s8, s2
	v_mfma_f32_16x16x32_bf16 v[46:49], v[6:9], v[34:37], v[94:97]
	s_addc_u32 s3, s9, 0
	v_mfma_f32_16x16x32_bf16 v[90:93], v[10:13], v[34:37], v[90:93]
	v_mfma_f32_16x16x32_bf16 v[86:89], v[14:17], v[34:37], v[86:89]
	v_mfma_f32_16x16x32_bf16 v[34:37], v[18:21], v[34:37], v[82:85]
	ds_read_b128 v[82:85], v110 offset:0x1800
	s_waitcnt lgkmcnt(2)
	s_nop 0
	v_mfma_f32_16x16x32_bf16 v[78:81], v[6:9], v[38:41], v[78:81]
	v_mfma_f32_16x16x32_bf16 v[74:77], v[10:13], v[38:41], v[74:77]
	v_mfma_f32_16x16x32_bf16 v[70:73], v[14:17], v[38:41], v[70:73]
	v_mfma_f32_16x16x32_bf16 v[38:41], v[18:21], v[38:41], v[66:69]
	s_waitcnt lgkmcnt(1)
	s_nop 0
	v_mfma_f32_16x16x32_bf16 v[62:65], v[6:9], v[42:45], v[62:65]
	v_mfma_f32_16x16x32_bf16 v[58:61], v[10:13], v[42:45], v[58:61]
	v_mfma_f32_16x16x32_bf16 v[54:57], v[14:17], v[42:45], v[54:57]
	v_mfma_f32_16x16x32_bf16 v[42:45], v[18:21], v[42:45], v[50:53]
	s_waitcnt lgkmcnt(0)
	s_nop 0
	v_mfma_f32_16x16x32_bf16 v[50:53], v[6:9], v[82:85], v[22:25]
	v_mfma_f32_16x16x32_bf16 v[66:69], v[10:13], v[82:85], v[26:29]
	v_mfma_f32_16x16x32_bf16 v[94:97], v[14:17], v[82:85], v[30:33]
	v_mfma_f32_16x16x32_bf16 v[2:5], v[18:21], v[82:85], v[2:5]
	ds_read_b128 v[18:21], v102 offset:0x400
	ds_read_b128 v[82:85], v102 offset:0xc00
	ds_read_b128 v[98:101], v102 offset:0x1400
	ds_read_b128 v[102:105], v102 offset:0x1c00
	ds_read_b128 v[6:9], v110 offset:0x400
	ds_read_b128 v[10:13], v110 offset:0xc00
	ds_read_b128 v[106:109], v110 offset:0x1400
	s_nop 0
	s_waitcnt lgkmcnt(2)
	s_nop 0
	v_mfma_f32_16x16x32_bf16 v[46:49], v[18:21], v[6:9], v[46:49]
	v_mfma_f32_16x16x32_bf16 v[90:93], v[82:85], v[6:9], v[90:93]
	v_mfma_f32_16x16x32_bf16 v[30:33], v[98:101], v[6:9], v[86:89]
	v_mfma_f32_16x16x32_bf16 v[14:17], v[102:105], v[6:9], v[34:37]
	ds_read_b128 v[86:89], v110 offset:0x1c00
	s_waitcnt lgkmcnt(2)
	s_nop 0
	v_mfma_f32_16x16x32_bf16 v[78:81], v[18:21], v[10:13], v[78:81]
	v_mfma_f32_16x16x32_bf16 v[74:77], v[82:85], v[10:13], v[74:77]
	v_mfma_f32_16x16x32_bf16 v[26:29], v[98:101], v[10:13], v[70:73]
	v_mfma_f32_16x16x32_bf16 v[10:13], v[102:105], v[10:13], v[38:41]
	s_waitcnt lgkmcnt(1)
	s_nop 0
	v_mfma_f32_16x16x32_bf16 v[62:65], v[18:21], v[106:109], v[62:65]
	v_mfma_f32_16x16x32_bf16 v[38:41], v[82:85], v[106:109], v[58:61]
	v_mfma_f32_16x16x32_bf16 v[22:25], v[98:101], v[106:109], v[54:57]
	v_mfma_f32_16x16x32_bf16 v[6:9], v[102:105], v[106:109], v[42:45]
	s_waitcnt lgkmcnt(0)
	s_nop 0
	v_mfma_f32_16x16x32_bf16 v[42:45], v[18:21], v[86:89], v[50:53]
	v_mfma_f32_16x16x32_bf16 v[34:37], v[82:85], v[86:89], v[66:69]
	v_mfma_f32_16x16x32_bf16 v[18:21], v[98:101], v[86:89], v[94:97]
	v_mfma_f32_16x16x32_bf16 v[2:5], v[102:105], v[86:89], v[2:5]
	v_lshrrev_b32_e32 v50, 2, v119
	v_and_b32_e32 v50, 12, v50
	v_lshl_or_b32 v66, v121, 6, v50
	v_lshlrev_b32_e32 v67, 2, v66
	s_waitcnt lgkmcnt(0)
	s_barrier
	global_load_dwordx4 v[50:53], v67, s[2:3]
	global_load_dwordx4 v[54:57], v67, s[2:3] offset:64
	v_lshrrev_b32_e32 v58, 1, v119
	v_lshl_or_b32 v59, v120, 6, v118
	v_and_b32_e32 v68, 8, v58
	v_lshl_add_u32 v69, v59, 9, 0
	v_or_b32_e32 v70, 16, v59
	v_or_b32_e32 v71, 48, v59
	v_lshrrev_b32_e32 v58, 3, v66
	v_or_b32_e32 v59, 16, v66
	v_bitop3_b32 v83, v70, v58, 31 bitop3:0x6c
	v_lshrrev_b32_e32 v85, 3, v59
	v_lshl_add_u32 v72, v70, 9, 0
	v_xor_b32_e32 v82, v58, v118
	v_bitop3_b32 v84, v71, v58, 31 bitop3:0x6c
	v_lshlrev_b32_e32 v83, 4, v83
	v_xor_b32_e32 v86, v85, v118
	v_lshl_add_u32 v73, v71, 9, 0
	v_lshlrev_b32_e32 v82, 4, v82
	v_lshlrev_b32_e32 v84, 4, v84
	v_add3_u32 v83, v72, v83, v68
	v_lshlrev_b32_e32 v86, 4, v86
	global_load_dwordx4 v[58:61], v67, s[2:3] offset:128
	v_add3_u32 v82, v69, v82, v68
	v_add3_u32 v84, v73, v84, v68
	v_add3_u32 v86, v69, v86, v68
	s_waitcnt vmcnt(2)
	v_add_f32_e32 v46, v46, v50
	v_add_f32_e32 v47, v47, v51
	v_add_f32_e32 v48, v48, v52
	v_add_f32_e32 v49, v49, v53
	v_add_f32_e32 v78, v78, v50
	v_add_f32_e32 v79, v79, v51
	v_add_f32_e32 v80, v80, v52
	v_add_f32_e32 v81, v81, v53
	v_add_f32_e32 v62, v62, v50
	v_add_f32_e32 v63, v63, v51
	v_add_f32_e32 v42, v42, v50
	v_add_f32_e32 v43, v43, v51
	v_add_f32_e32 v44, v44, v52
	v_add_f32_e32 v45, v45, v53
	s_waitcnt vmcnt(1)
	v_add_f32_e32 v50, v90, v54
	v_add_f32_e32 v51, v91, v55
	v_add_f32_e32 v64, v64, v52
	v_add_f32_e32 v65, v65, v53
	v_add_f32_e32 v52, v92, v56
	v_add_f32_e32 v53, v93, v57
	v_max_f32_e32 v46, 0, v46
	v_max_f32_e32 v47, 0, v47
	v_max_f32_e32 v48, 0, v48
	v_max_f32_e32 v49, 0, v49
	v_max_f32_e32 v78, 0, v78
	v_max_f32_e32 v79, 0, v79
	v_max_f32_e32 v80, 0, v80
	v_max_f32_e32 v81, 0, v81
	v_max_f32_e32 v88, 0, v43
	v_max_f32_e32 v89, 0, v44
	v_max_f32_e32 v90, 0, v45
	v_max_f32_e32 v50, 0, v50
	v_max_f32_e32 v51, 0, v51
	v_cvt_pk_bf16_f32 v43, v48, v49
	v_cvt_pk_bf16_f32 v44, v78, v79
	v_cvt_pk_bf16_f32 v45, v80, v81
	v_max_f32_e32 v62, 0, v62
	v_max_f32_e32 v63, 0, v63
	v_max_f32_e32 v64, 0, v64
	v_max_f32_e32 v65, 0, v65
	v_max_f32_e32 v87, 0, v42
	v_max_f32_e32 v52, 0, v52
	v_max_f32_e32 v53, 0, v53
	v_cvt_pk_bf16_f32 v42, v46, v47
	v_cvt_pk_bf16_f32 v46, v62, v63
	v_cvt_pk_bf16_f32 v47, v64, v65
	v_cvt_pk_bf16_f32 v48, v87, v88
	v_cvt_pk_bf16_f32 v49, v89, v90
	v_cvt_pk_bf16_f32 v50, v50, v51
	v_cvt_pk_bf16_f32 v51, v52, v53
	ds_write_b64 v83, v[44:45]
	ds_write2st64_b64 v82, v[42:43], v[46:47] offset1:32
	ds_write_b64 v84, v[48:49]
	ds_write_b64 v86, v[50:51]
	v_add_f32_e32 v43, v76, v56
	v_add_f32_e32 v44, v77, v57
	v_max_f32_e32 v43, 0, v43
	v_max_f32_e32 v44, 0, v44
	v_add_f32_e32 v42, v75, v55
	v_cvt_pk_bf16_f32 v43, v43, v44
	v_bitop3_b32 v44, v85, v70, 31 bitop3:0x78
	v_add_f32_e32 v74, v74, v54
	v_max_f32_e32 v42, 0, v42
	v_lshlrev_b32_e32 v44, 4, v44
	v_max_f32_e32 v74, 0, v74
	v_cvt_pk_bf16_f32 v42, v74, v42
	v_add3_u32 v44, v72, v44, v68
	ds_write_b64 v44, v[42:43]
	global_load_dwordx4 v[42:45], v67, s[2:3] offset:192
	v_add_f32_e32 v34, v34, v54
	v_add_f32_e32 v35, v35, v55
	v_add_f32_e32 v36, v36, v56
	v_max_f32_e32 v34, 0, v34
	v_max_f32_e32 v35, 0, v35
	v_max_f32_e32 v36, 0, v36
	v_add_f32_e32 v37, v37, v57
	v_max_f32_e32 v37, 0, v37
	v_cvt_pk_bf16_f32 v34, v34, v35
	v_cvt_pk_bf16_f32 v35, v36, v37
	v_bitop3_b32 v36, v85, v71, 31 bitop3:0x78
	v_add_f32_e32 v38, v38, v54
	v_add_f32_e32 v39, v39, v55
	v_lshlrev_b32_e32 v36, 4, v36
	v_max_f32_e32 v38, 0, v38
	v_max_f32_e32 v39, 0, v39
	v_add_f32_e32 v40, v40, v56
	v_add_f32_e32 v41, v41, v57
	v_add3_u32 v36, v73, v36, v68
	v_max_f32_e32 v40, 0, v40
	v_max_f32_e32 v41, 0, v41
	v_cvt_pk_bf16_f32 v38, v38, v39
	v_cvt_pk_bf16_f32 v39, v40, v41
	ds_write_b64 v86, v[38:39] offset:16384
	ds_write_b64 v36, v[34:35]
	v_or_b32_e32 v34, 32, v66
	s_waitcnt vmcnt(1)
	v_add_f32_e32 v30, v30, v58
	v_add_f32_e32 v31, v31, v59
	v_add_f32_e32 v32, v32, v60
	v_add_f32_e32 v26, v26, v58
	v_add_f32_e32 v27, v27, v59
	v_add_f32_e32 v28, v28, v60
	v_add_f32_e32 v18, v18, v58
	v_add_f32_e32 v19, v19, v59
	v_add_f32_e32 v20, v20, v60
	v_lshrrev_b32_e32 v34, 3, v34
	v_max_f32_e32 v30, 0, v30
	v_max_f32_e32 v31, 0, v31
	v_max_f32_e32 v32, 0, v32
	v_add_f32_e32 v33, v33, v61
	v_max_f32_e32 v26, 0, v26
	v_max_f32_e32 v27, 0, v27
	v_max_f32_e32 v28, 0, v28
	v_add_f32_e32 v29, v29, v61
	v_max_f32_e32 v18, 0, v18
	v_max_f32_e32 v19, 0, v19
	v_max_f32_e32 v20, 0, v20
	v_add_f32_e32 v21, v21, v61
	v_max_f32_e32 v33, 0, v33
	v_cvt_pk_bf16_f32 v30, v30, v31
	v_cvt_pk_bf16_f32 v31, v32, v33
	v_xor_b32_e32 v32, v34, v118
	v_max_f32_e32 v29, 0, v29
	v_cvt_pk_bf16_f32 v26, v26, v27
	v_cvt_pk_bf16_f32 v27, v28, v29
	v_bitop3_b32 v28, v34, v70, 31 bitop3:0x78
	v_max_f32_e32 v21, 0, v21
	v_cvt_pk_bf16_f32 v18, v18, v19
	v_cvt_pk_bf16_f32 v19, v20, v21
	v_bitop3_b32 v20, v34, v71, 31 bitop3:0x78
	v_lshlrev_b32_e32 v32, 4, v32
	v_lshlrev_b32_e32 v28, 4, v28
	v_add_f32_e32 v22, v22, v58
	v_add_f32_e32 v23, v23, v59
	v_lshlrev_b32_e32 v20, 4, v20
	v_add3_u32 v32, v69, v32, v68
	v_add3_u32 v28, v72, v28, v68
	v_max_f32_e32 v22, 0, v22
	v_max_f32_e32 v23, 0, v23
	v_add_f32_e32 v24, v24, v60
	v_add_f32_e32 v25, v25, v61
	v_add3_u32 v20, v73, v20, v68
	ds_write_b64 v32, v[30:31]
	ds_write_b64 v28, v[26:27]
	v_max_f32_e32 v24, 0, v24
	v_max_f32_e32 v25, 0, v25
	v_cvt_pk_bf16_f32 v22, v22, v23
	v_cvt_pk_bf16_f32 v23, v24, v25
	ds_write_b64 v32, v[22:23] offset:16384
	ds_write_b64 v20, v[18:19]
	v_or_b32_e32 v18, 48, v66
	s_waitcnt vmcnt(0)
	v_add_f32_e32 v14, v14, v42
	v_add_f32_e32 v15, v15, v43
	v_add_f32_e32 v16, v16, v44
	v_add_f32_e32 v10, v10, v42
	v_add_f32_e32 v11, v11, v43
	v_add_f32_e32 v12, v12, v44
	v_add_f32_e32 v2, v2, v42
	v_add_f32_e32 v3, v3, v43
	v_add_f32_e32 v4, v4, v44
	v_lshrrev_b32_e32 v18, 3, v18
	v_max_f32_e32 v14, 0, v14
	v_max_f32_e32 v15, 0, v15
	v_max_f32_e32 v16, 0, v16
	v_add_f32_e32 v17, v17, v45
	v_max_f32_e32 v10, 0, v10
	v_max_f32_e32 v11, 0, v11
	v_max_f32_e32 v12, 0, v12
	v_add_f32_e32 v13, v13, v45
	v_max_f32_e32 v2, 0, v2
	v_max_f32_e32 v3, 0, v3
	v_max_f32_e32 v4, 0, v4
	v_add_f32_e32 v5, v5, v45
	v_max_f32_e32 v17, 0, v17
	v_cvt_pk_bf16_f32 v14, v14, v15
	v_cvt_pk_bf16_f32 v15, v16, v17
	v_xor_b32_e32 v16, v18, v118
	v_max_f32_e32 v13, 0, v13
	v_cvt_pk_bf16_f32 v10, v10, v11
	v_cvt_pk_bf16_f32 v11, v12, v13
	v_bitop3_b32 v12, v18, v70, 31 bitop3:0x78
	v_max_f32_e32 v5, 0, v5
	v_cvt_pk_bf16_f32 v2, v2, v3
	v_cvt_pk_bf16_f32 v3, v4, v5
	v_bitop3_b32 v4, v18, v71, 31 bitop3:0x78
	v_lshlrev_b32_e32 v16, 4, v16
	v_lshlrev_b32_e32 v12, 4, v12
	v_add_f32_e32 v6, v6, v42
	v_add_f32_e32 v7, v7, v43
	v_lshlrev_b32_e32 v4, 4, v4
	v_add3_u32 v16, v69, v16, v68
	v_add3_u32 v12, v72, v12, v68
	v_max_f32_e32 v6, 0, v6
	v_max_f32_e32 v7, 0, v7
	v_add_f32_e32 v8, v8, v44
	v_add_f32_e32 v9, v9, v45
	v_add3_u32 v4, v73, v4, v68
	ds_write_b64 v16, v[14:15]
	ds_write_b64 v12, v[10:11]
	v_max_f32_e32 v8, 0, v8
	v_max_f32_e32 v9, 0, v9
	v_cvt_pk_bf16_f32 v6, v6, v7
	v_cvt_pk_bf16_f32 v7, v8, v9
	ds_write_b64 v16, v[6:7] offset:16384
	ds_write_b64 v4, v[2:3]
	v_and_b32_e32 v2, 0x1f0, v1
	v_mov_b32_e32 v3, 0
	v_lshl_add_u64 v[12:13], s[0:1], 0, v[2:3]
	s_mov_b64 s[0:1], 0x2000000
	v_lshl_add_u64 v[12:13], v[12:13], 0, s[0:1]
	v_lshrrev_b32_e32 v1, 5, v0
	s_waitcnt lgkmcnt(0)
	s_barrier
	v_mov_b32_e32 v4, v1
	v_xor_b32_e32 v5, v4, v0
	v_lshlrev_b32_e32 v5, 4, v5
	v_and_b32_e32 v5, 0x1f0, v5
	v_lshl_add_u32 v6, v4, 9, v5
	ds_read_b128 v[192:195], v6
	v_lshlrev_b32_e32 v2, 11, v4
	v_lshl_add_u64 v[160:161], v[12:13], 0, v[2:3]
	v_or_b32_e32 v4, 0x10, v1
	v_xor_b32_e32 v5, v4, v0
	v_lshlrev_b32_e32 v5, 4, v5
	v_and_b32_e32 v5, 0x1f0, v5
	v_lshl_add_u32 v6, v4, 9, v5
	ds_read_b128 v[196:199], v6
	v_lshlrev_b32_e32 v2, 11, v4
	v_lshl_add_u64 v[162:163], v[12:13], 0, v[2:3]
	v_or_b32_e32 v4, 0x20, v1
	v_xor_b32_e32 v5, v4, v0
	v_lshlrev_b32_e32 v5, 4, v5
	v_and_b32_e32 v5, 0x1f0, v5
	v_lshl_add_u32 v6, v4, 9, v5
	ds_read_b128 v[200:203], v6
	v_lshlrev_b32_e32 v2, 11, v4
	v_lshl_add_u64 v[164:165], v[12:13], 0, v[2:3]
	v_or_b32_e32 v4, 0x30, v1
	v_xor_b32_e32 v5, v4, v0
	v_lshlrev_b32_e32 v5, 4, v5
	v_and_b32_e32 v5, 0x1f0, v5
	v_lshl_add_u32 v6, v4, 9, v5
	ds_read_b128 v[204:207], v6
	v_lshlrev_b32_e32 v2, 11, v4
	v_lshl_add_u64 v[166:167], v[12:13], 0, v[2:3]
	v_or_b32_e32 v4, 0x40, v1
	v_xor_b32_e32 v5, v4, v0
	v_lshlrev_b32_e32 v5, 4, v5
	v_and_b32_e32 v5, 0x1f0, v5
	v_lshl_add_u32 v6, v4, 9, v5
	ds_read_b128 v[208:211], v6
	v_lshlrev_b32_e32 v2, 11, v4
	v_lshl_add_u64 v[168:169], v[12:13], 0, v[2:3]
	v_or_b32_e32 v4, 0x50, v1
	v_xor_b32_e32 v5, v4, v0
	v_lshlrev_b32_e32 v5, 4, v5
	v_and_b32_e32 v5, 0x1f0, v5
	v_lshl_add_u32 v6, v4, 9, v5
	ds_read_b128 v[212:215], v6
	v_lshlrev_b32_e32 v2, 11, v4
	v_lshl_add_u64 v[170:171], v[12:13], 0, v[2:3]
	v_or_b32_e32 v4, 0x60, v1
	v_xor_b32_e32 v5, v4, v0
	v_lshlrev_b32_e32 v5, 4, v5
	v_and_b32_e32 v5, 0x1f0, v5
	v_lshl_add_u32 v6, v4, 9, v5
	ds_read_b128 v[216:219], v6
	v_lshlrev_b32_e32 v2, 11, v4
	v_lshl_add_u64 v[172:173], v[12:13], 0, v[2:3]
	v_or_b32_e32 v4, 0x70, v1
	v_xor_b32_e32 v5, v4, v0
	v_lshlrev_b32_e32 v5, 4, v5
	v_and_b32_e32 v5, 0x1f0, v5
	v_lshl_add_u32 v6, v4, 9, v5
	ds_read_b128 v[220:223], v6
	v_lshlrev_b32_e32 v2, 11, v4
	v_lshl_add_u64 v[174:175], v[12:13], 0, v[2:3]
	s_waitcnt lgkmcnt(7)
	global_store_dwordx4 v[160:161], v[192:195], off sc1
	s_waitcnt lgkmcnt(6)
	global_store_dwordx4 v[162:163], v[196:199], off sc1
	s_waitcnt lgkmcnt(5)
	global_store_dwordx4 v[164:165], v[200:203], off sc1
	s_waitcnt lgkmcnt(4)
	global_store_dwordx4 v[166:167], v[204:207], off sc1
	s_waitcnt lgkmcnt(3)
	global_store_dwordx4 v[168:169], v[208:211], off sc1
	s_waitcnt lgkmcnt(2)
	global_store_dwordx4 v[170:171], v[212:215], off sc1
	s_waitcnt lgkmcnt(1)
	global_store_dwordx4 v[172:173], v[216:219], off sc1
	s_waitcnt lgkmcnt(0)
	global_store_dwordx4 v[174:175], v[220:223], off sc1
	s_endpgm

	.amdhsa_kernel _Z9proj_gemmPKfS0_S0_PK14__hip_bfloat16S0_S0_S0_PS1_
		.amdhsa_group_segment_fixed_size 0
		.amdhsa_private_segment_fixed_size 0
		.amdhsa_kernarg_size 64
		.amdhsa_user_sgpr_count 2
		.amdhsa_user_sgpr_dispatch_ptr 0
		.amdhsa_user_sgpr_queue_ptr 0
		.amdhsa_user_sgpr_kernarg_segment_ptr 1
		.amdhsa_user_sgpr_dispatch_id 0
		.amdhsa_user_sgpr_kernarg_preload_length 0
		.amdhsa_user_sgpr_kernarg_preload_offset 0
		.amdhsa_user_sgpr_private_segment_size 0
		.amdhsa_uses_dynamic_stack 0
		.amdhsa_enable_private_segment 0
		.amdhsa_system_sgpr_workgroup_id_x 1
		.amdhsa_system_sgpr_workgroup_id_y 0
		.amdhsa_system_sgpr_workgroup_id_z 0
		.amdhsa_system_sgpr_workgroup_info 0
		.amdhsa_system_vgpr_workitem_id 0
		.amdhsa_next_free_vgpr 256
		.amdhsa_next_free_sgpr 40
		.amdhsa_accum_offset 256
		.amdhsa_reserve_vcc 0
		.amdhsa_float_round_mode_32 0
		.amdhsa_float_round_mode_16_64 0
		.amdhsa_float_denorm_mode_32 3
		.amdhsa_float_denorm_mode_16_64 3
		.amdhsa_dx10_clamp 1
		.amdhsa_ieee_mode 1
		.amdhsa_fp16_overflow 0
		.amdhsa_tg_split 0
		.amdhsa_exception_fp_ieee_invalid_op 0
		.amdhsa_exception_fp_denorm_src 0
		.amdhsa_exception_fp_ieee_div_zero 0
		.amdhsa_exception_fp_ieee_overflow 0
		.amdhsa_exception_fp_ieee_underflow 0
		.amdhsa_exception_fp_ieee_inexact 0
		.amdhsa_exception_int_div_zero 0
	.end_amdhsa_kernel
